# fp8 GEMM MFMA blocks: redundant lgkmcnt(0) at block start removed, mid-block priority toggle removed, closing priority drop moved behind the barrier
# speedup vs baseline: 1.0025x; 1.0025x over previous
.LBB0_258:
	s_lshl_b64 s[2:3], s[82:83], 7
	s_add_u32 s26, s4, s2
	v_mov_b32_e32 v2, v184
	v_readfirstlane_b32 s28, v187
	ds_read_b128 v[218:221], v214 offset:16384
	ds_read_b128 v[222:225], v214 offset:17408
	ds_read_b128 v[226:229], v215 offset:16384
	ds_read_b128 v[230:233], v215 offset:17408
	ds_read_b128 v[234:237], v216 offset:16384
	ds_read_b128 v[238:241], v216 offset:17408
	ds_read_b128 v[242:245], v217 offset:16384
	ds_read_b128 v[246:249], v217 offset:17408
	s_addc_u32 s27, s5, s3
	s_mov_b32 m0, s28
	s_add_u32 s28, s26, 0x10000
	global_load_lds_dwordx4 v2, s[26:27]
	v_mov_b32_e32 v2, v184
	v_readfirstlane_b32 s30, v188
	s_addc_u32 s29, s27, 0
	s_mov_b32 m0, s30
	v_readfirstlane_b32 s30, v189
	global_load_lds_dwordx4 v2, s[28:29]
	s_add_u32 s28, s26, 0x20000
	v_mov_b32_e32 v2, v184
	s_addc_u32 s29, s27, 0
	s_mov_b32 m0, s30
	s_add_u32 s26, s26, 0x30000
	global_load_lds_dwordx4 v2, s[28:29]
	v_mov_b32_e32 v2, v184
	v_readfirstlane_b32 s28, v190
	s_addc_u32 s27, s27, 0
	s_mov_b32 m0, s28
	s_add_u32 s2, s6, s2
	global_load_lds_dwordx4 v2, s[26:27]
	v_mov_b32_e32 v2, v180
	v_readfirstlane_b32 s26, v191
	s_addc_u32 s3, s7, s3
	s_mov_b32 m0, s26
	v_readfirstlane_b32 s26, v201
	global_load_lds_dwordx4 v2, s[2:3]
	v_mov_b32_e32 v2, v181
	s_mov_b32 m0, s26
	s_nop 0
	global_load_lds_dwordx4 v2, s[2:3]
	s_waitcnt vmcnt(8)
	s_waitcnt lgkmcnt(0)
	s_barrier
	s_setprio 1
	v_mfma_scale_f32_16x16x128_f8f6f4 v[144:147], v[20:27], v[218:225], v[144:147], v186, v185 op_sel_hi:[0,0,0]
	v_mfma_scale_f32_16x16x128_f8f6f4 v[140:143], v[28:35], v[218:225], v[140:143], v186, v185 op_sel_hi:[0,0,0]
	v_mfma_scale_f32_16x16x128_f8f6f4 v[136:139], v[20:27], v[226:233], v[136:139], v186, v185 op_sel_hi:[0,0,0]
	v_mfma_scale_f32_16x16x128_f8f6f4 v[132:135], v[28:35], v[226:233], v[132:135], v186, v185 op_sel_hi:[0,0,0]
	v_mfma_scale_f32_16x16x128_f8f6f4 v[128:131], v[20:27], v[234:241], v[128:131], v186, v185 op_sel_hi:[0,0,0]
	v_mfma_scale_f32_16x16x128_f8f6f4 v[124:127], v[28:35], v[234:241], v[124:127], v186, v185 op_sel_hi:[0,0,0]
	v_mfma_scale_f32_16x16x128_f8f6f4 v[120:123], v[20:27], v[242:249], v[120:123], v186, v185 op_sel_hi:[0,0,0]
	v_mfma_scale_f32_16x16x128_f8f6f4 v[116:119], v[28:35], v[242:249], v[116:119], v186, v185 op_sel_hi:[0,0,0]
	v_mfma_scale_f32_16x16x128_f8f6f4 v[80:83], v[4:11], v[218:225], v[80:83], v186, v185 op_sel_hi:[0,0,0]
	v_mfma_scale_f32_16x16x128_f8f6f4 v[76:79], v[12:19], v[218:225], v[76:79], v186, v185 op_sel_hi:[0,0,0]
	v_mfma_scale_f32_16x16x128_f8f6f4 v[72:75], v[4:11], v[226:233], v[72:75], v186, v185 op_sel_hi:[0,0,0]
	v_mfma_scale_f32_16x16x128_f8f6f4 v[68:71], v[12:19], v[226:233], v[68:71], v186, v185 op_sel_hi:[0,0,0]
	v_mfma_scale_f32_16x16x128_f8f6f4 v[64:67], v[4:11], v[234:241], v[64:67], v186, v185 op_sel_hi:[0,0,0]
	v_mfma_scale_f32_16x16x128_f8f6f4 v[60:63], v[12:19], v[234:241], v[60:63], v186, v185 op_sel_hi:[0,0,0]
	v_mfma_scale_f32_16x16x128_f8f6f4 v[56:59], v[4:11], v[242:249], v[56:59], v186, v185 op_sel_hi:[0,0,0]
	v_mfma_scale_f32_16x16x128_f8f6f4 v[52:55], v[12:19], v[242:249], v[52:55], v186, v185 op_sel_hi:[0,0,0]
	s_barrier
	s_setprio 0
	ds_read_b128 v[20:23], v212
	ds_read_b128 v[24:27], v212 offset:1024
	ds_read_b128 v[28:31], v212 offset:2048
	ds_read_b128 v[32:35], v212 offset:3072
	ds_read_b128 v[4:7], v213
	ds_read_b128 v[8:11], v213 offset:1024
	ds_read_b128 v[12:15], v213 offset:2048
	ds_read_b128 v[16:19], v213 offset:3072
	v_mov_b32_e32 v2, v182
	v_readfirstlane_b32 s26, v202
	ds_read_b128 v[218:221], v214 offset:32768
	ds_read_b128 v[222:225], v214 offset:33792
	ds_read_b128 v[226:229], v215 offset:32768
	ds_read_b128 v[230:233], v215 offset:33792
	ds_read_b128 v[234:237], v216 offset:32768
	ds_read_b128 v[238:241], v216 offset:33792
	ds_read_b128 v[242:245], v217 offset:32768
	ds_read_b128 v[246:249], v217 offset:33792
	s_mov_b32 m0, s26
	v_readfirstlane_b32 s26, v203
	global_load_lds_dwordx4 v2, s[2:3]
	v_mov_b32_e32 v2, v183
	s_mov_b32 m0, s26
	s_nop 0
	global_load_lds_dwordx4 v2, s[2:3]
	s_waitcnt vmcnt(8)
	s_waitcnt lgkmcnt(0)
	s_barrier
	s_setprio 1
	v_mfma_scale_f32_16x16x128_f8f6f4 v[176:179], v[20:27], v[218:225], v[176:179], v186, v185 op_sel_hi:[0,0,0]
	v_mfma_scale_f32_16x16x128_f8f6f4 v[172:175], v[28:35], v[218:225], v[172:175], v186, v185 op_sel_hi:[0,0,0]
	v_mfma_scale_f32_16x16x128_f8f6f4 v[168:171], v[20:27], v[226:233], v[168:171], v186, v185 op_sel_hi:[0,0,0]
	v_mfma_scale_f32_16x16x128_f8f6f4 v[164:167], v[28:35], v[226:233], v[164:167], v186, v185 op_sel_hi:[0,0,0]
	v_mfma_scale_f32_16x16x128_f8f6f4 v[160:163], v[20:27], v[234:241], v[160:163], v186, v185 op_sel_hi:[0,0,0]
	v_mfma_scale_f32_16x16x128_f8f6f4 v[156:159], v[28:35], v[234:241], v[156:159], v186, v185 op_sel_hi:[0,0,0]
	v_mfma_scale_f32_16x16x128_f8f6f4 v[152:155], v[20:27], v[242:249], v[152:155], v186, v185 op_sel_hi:[0,0,0]
	v_mfma_scale_f32_16x16x128_f8f6f4 v[148:151], v[28:35], v[242:249], v[148:151], v186, v185 op_sel_hi:[0,0,0]
	v_mfma_scale_f32_16x16x128_f8f6f4 v[112:115], v[4:11], v[218:225], v[112:115], v186, v185 op_sel_hi:[0,0,0]
	v_mfma_scale_f32_16x16x128_f8f6f4 v[108:111], v[12:19], v[218:225], v[108:111], v186, v185 op_sel_hi:[0,0,0]
	v_mfma_scale_f32_16x16x128_f8f6f4 v[104:107], v[4:11], v[226:233], v[104:107], v186, v185 op_sel_hi:[0,0,0]
	v_mfma_scale_f32_16x16x128_f8f6f4 v[100:103], v[12:19], v[226:233], v[100:103], v186, v185 op_sel_hi:[0,0,0]
	v_mfma_scale_f32_16x16x128_f8f6f4 v[96:99], v[4:11], v[234:241], v[96:99], v186, v185 op_sel_hi:[0,0,0]
	v_mfma_scale_f32_16x16x128_f8f6f4 v[92:95], v[12:19], v[234:241], v[92:95], v186, v185 op_sel_hi:[0,0,0]
	v_mfma_scale_f32_16x16x128_f8f6f4 v[88:91], v[4:11], v[242:249], v[88:91], v186, v185 op_sel_hi:[0,0,0]
	v_mfma_scale_f32_16x16x128_f8f6f4 v[84:87], v[12:19], v[242:249], v[84:87], v186, v185 op_sel_hi:[0,0,0]
	s_barrier
	s_setprio 0
	s_add_i32 s82, s82, 1
	s_lshl_b64 s[2:3], s[82:83], 7
	s_add_u32 s26, s4, s2
	v_mov_b32_e32 v2, v184
	v_readfirstlane_b32 s28, v204
	ds_read_b128 v[218:221], v214 offset:49152
	ds_read_b128 v[222:225], v214 offset:50176
	ds_read_b128 v[226:229], v215 offset:49152
	ds_read_b128 v[230:233], v215 offset:50176
	ds_read_b128 v[234:237], v216 offset:49152
	ds_read_b128 v[238:241], v216 offset:50176
	ds_read_b128 v[242:245], v217 offset:49152
	ds_read_b128 v[246:249], v217 offset:50176
	s_addc_u32 s27, s5, s3
	s_mov_b32 m0, s28
	s_add_u32 s28, s26, 0x10000
	global_load_lds_dwordx4 v2, s[26:27]
	v_mov_b32_e32 v2, v184
	v_readfirstlane_b32 s30, v205
	s_addc_u32 s29, s27, 0
	s_mov_b32 m0, s30
	v_readfirstlane_b32 s30, v208
	global_load_lds_dwordx4 v2, s[28:29]
	s_add_u32 s28, s26, 0x20000
	v_mov_b32_e32 v2, v184
	s_addc_u32 s29, s27, 0
	s_mov_b32 m0, s30
	s_add_u32 s26, s26, 0x30000
	global_load_lds_dwordx4 v2, s[28:29]
	v_mov_b32_e32 v2, v184
	v_readfirstlane_b32 s28, v209
	s_addc_u32 s27, s27, 0
	s_mov_b32 m0, s28
	s_add_u32 s2, s6, s2
	global_load_lds_dwordx4 v2, s[26:27]
	v_mov_b32_e32 v2, v180
	v_readfirstlane_b32 s26, v206
	s_addc_u32 s3, s7, s3
	s_mov_b32 m0, s26
	v_readfirstlane_b32 s26, v207
	global_load_lds_dwordx4 v2, s[2:3]
	v_mov_b32_e32 v2, v181
	s_mov_b32 m0, s26
	s_nop 0
	global_load_lds_dwordx4 v2, s[2:3]
	s_waitcnt vmcnt(8)
	s_waitcnt lgkmcnt(0)
	s_barrier
	s_setprio 1
	v_mfma_scale_f32_16x16x128_f8f6f4 v[144:147], v[20:27], v[218:225], v[144:147], v186, v185 op_sel_hi:[0,0,0]
	v_mfma_scale_f32_16x16x128_f8f6f4 v[140:143], v[28:35], v[218:225], v[140:143], v186, v185 op_sel_hi:[0,0,0]
	v_mfma_scale_f32_16x16x128_f8f6f4 v[136:139], v[20:27], v[226:233], v[136:139], v186, v185 op_sel_hi:[0,0,0]
	v_mfma_scale_f32_16x16x128_f8f6f4 v[132:135], v[28:35], v[226:233], v[132:135], v186, v185 op_sel_hi:[0,0,0]
	v_mfma_scale_f32_16x16x128_f8f6f4 v[128:131], v[20:27], v[234:241], v[128:131], v186, v185 op_sel_hi:[0,0,0]
	v_mfma_scale_f32_16x16x128_f8f6f4 v[124:127], v[28:35], v[234:241], v[124:127], v186, v185 op_sel_hi:[0,0,0]
	v_mfma_scale_f32_16x16x128_f8f6f4 v[120:123], v[20:27], v[242:249], v[120:123], v186, v185 op_sel_hi:[0,0,0]
	v_mfma_scale_f32_16x16x128_f8f6f4 v[116:119], v[28:35], v[242:249], v[116:119], v186, v185 op_sel_hi:[0,0,0]
	v_mfma_scale_f32_16x16x128_f8f6f4 v[80:83], v[4:11], v[218:225], v[80:83], v186, v185 op_sel_hi:[0,0,0]
	v_mfma_scale_f32_16x16x128_f8f6f4 v[76:79], v[12:19], v[218:225], v[76:79], v186, v185 op_sel_hi:[0,0,0]
	v_mfma_scale_f32_16x16x128_f8f6f4 v[72:75], v[4:11], v[226:233], v[72:75], v186, v185 op_sel_hi:[0,0,0]
	v_mfma_scale_f32_16x16x128_f8f6f4 v[68:71], v[12:19], v[226:233], v[68:71], v186, v185 op_sel_hi:[0,0,0]
	v_mfma_scale_f32_16x16x128_f8f6f4 v[64:67], v[4:11], v[234:241], v[64:67], v186, v185 op_sel_hi:[0,0,0]
	v_mfma_scale_f32_16x16x128_f8f6f4 v[60:63], v[12:19], v[234:241], v[60:63], v186, v185 op_sel_hi:[0,0,0]
	v_mfma_scale_f32_16x16x128_f8f6f4 v[56:59], v[4:11], v[242:249], v[56:59], v186, v185 op_sel_hi:[0,0,0]
	v_mfma_scale_f32_16x16x128_f8f6f4 v[52:55], v[12:19], v[242:249], v[52:55], v186, v185 op_sel_hi:[0,0,0]
	s_barrier
	s_setprio 0
	s_add_i32 s25, s25, 2
	s_add_u32 s12, s12, 0x100
	s_addc_u32 s13, s13, 0
	s_cmp_gt_u32 s25, 5
	s_cbranch_scc1 .LBB0_263
.LBB0_259:
	ds_read_b128 v[20:23], v210
	ds_read_b128 v[24:27], v210 offset:1024
	ds_read_b128 v[28:31], v210 offset:2048
	ds_read_b128 v[32:35], v210 offset:3072
	ds_read_b128 v[4:7], v211
	ds_read_b128 v[8:11], v211 offset:1024
	ds_read_b128 v[12:15], v211 offset:2048
	ds_read_b128 v[16:19], v211 offset:3072
	s_add_u32 s2, s6, s12
	s_addc_u32 s3, s7, s13
	v_add_u32_e32 v192, 0xc000, v191
	s_add_u32 s2, s2, 0x80
	v_mov_b32_e32 v2, v182
	v_readfirstlane_b32 s26, v192
	v_add_u32_e32 v192, 0xe000, v191
	ds_read_b128 v[218:221], v214
	ds_read_b128 v[222:225], v214 offset:1024
	ds_read_b128 v[226:229], v215
	ds_read_b128 v[230:233], v215 offset:1024
	ds_read_b128 v[234:237], v216
	ds_read_b128 v[238:241], v216 offset:1024
	ds_read_b128 v[242:245], v217
	ds_read_b128 v[246:249], v217 offset:1024
	s_addc_u32 s3, s3, 0
	s_mov_b32 m0, s26
	v_readfirstlane_b32 s26, v192
	global_load_lds_dwordx4 v2, s[2:3]
	v_mov_b32_e32 v2, v183
	s_mov_b32 m0, s26
	s_nop 0
	global_load_lds_dwordx4 v2, s[2:3]
	s_waitcnt vmcnt(8)
	s_waitcnt lgkmcnt(0)
	s_barrier
	s_setprio 1
	v_mfma_scale_f32_16x16x128_f8f6f4 v[176:179], v[20:27], v[218:225], v[176:179], v186, v185 op_sel_hi:[0,0,0]
	v_mfma_scale_f32_16x16x128_f8f6f4 v[172:175], v[28:35], v[218:225], v[172:175], v186, v185 op_sel_hi:[0,0,0]
	v_mfma_scale_f32_16x16x128_f8f6f4 v[168:171], v[20:27], v[226:233], v[168:171], v186, v185 op_sel_hi:[0,0,0]
	v_mfma_scale_f32_16x16x128_f8f6f4 v[164:167], v[28:35], v[226:233], v[164:167], v186, v185 op_sel_hi:[0,0,0]
	v_mfma_scale_f32_16x16x128_f8f6f4 v[160:163], v[20:27], v[234:241], v[160:163], v186, v185 op_sel_hi:[0,0,0]
	v_mfma_scale_f32_16x16x128_f8f6f4 v[156:159], v[28:35], v[234:241], v[156:159], v186, v185 op_sel_hi:[0,0,0]
	v_mfma_scale_f32_16x16x128_f8f6f4 v[152:155], v[20:27], v[242:249], v[152:155], v186, v185 op_sel_hi:[0,0,0]
	v_mfma_scale_f32_16x16x128_f8f6f4 v[148:151], v[28:35], v[242:249], v[148:151], v186, v185 op_sel_hi:[0,0,0]
	v_mfma_scale_f32_16x16x128_f8f6f4 v[112:115], v[4:11], v[218:225], v[112:115], v186, v185 op_sel_hi:[0,0,0]
	v_mfma_scale_f32_16x16x128_f8f6f4 v[108:111], v[12:19], v[218:225], v[108:111], v186, v185 op_sel_hi:[0,0,0]
	v_mfma_scale_f32_16x16x128_f8f6f4 v[104:107], v[4:11], v[226:233], v[104:107], v186, v185 op_sel_hi:[0,0,0]
	v_mfma_scale_f32_16x16x128_f8f6f4 v[100:103], v[12:19], v[226:233], v[100:103], v186, v185 op_sel_hi:[0,0,0]
	v_mfma_scale_f32_16x16x128_f8f6f4 v[96:99], v[4:11], v[234:241], v[96:99], v186, v185 op_sel_hi:[0,0,0]
	v_mfma_scale_f32_16x16x128_f8f6f4 v[92:95], v[12:19], v[234:241], v[92:95], v186, v185 op_sel_hi:[0,0,0]
	v_mfma_scale_f32_16x16x128_f8f6f4 v[88:91], v[4:11], v[242:249], v[88:91], v186, v185 op_sel_hi:[0,0,0]
	v_mfma_scale_f32_16x16x128_f8f6f4 v[84:87], v[12:19], v[242:249], v[84:87], v186, v185 op_sel_hi:[0,0,0]
	s_cmp_lg_u32 s25, 4
	s_barrier
	s_setprio 0
	s_cbranch_scc1 .LBB0_262
	s_cmpk_gt_u32 s15, 0xd7f
	s_mov_b64 s[20:21], 0
	s_cbranch_scc1 .LBB0_257
	v_readlane_b32 s2, v255, 41
	v_readlane_b32 s4, v255, 40
	v_mov_b32_e32 v2, v0
	s_mov_b64 s[20:21], -1
	v_ashrrev_i32_e32 v181, 31, v2
	v_lshrrev_b32_e32 v181, 26, v181
	v_lshlrev_b32_e32 v180, 4, v2
	v_add_u32_e32 v181, v2, v181
	v_bfe_i32 v2, v2, 27, 1
	s_waitcnt lgkmcnt(0)
	s_lshr_b32 s2, s2, 16
	v_lshrrev_b32_e32 v2, 22, v2
	s_cmp_lg_u32 s2, 0
	v_add_u32_e32 v2, v180, v2
	s_cselect_b64 s[2:3], -1, 0
	v_and_b32_e32 v2, 0xfffffc00, v2
	s_cmp_lg_u64 s[2:3], 0
	v_sub_u32_e32 v2, v180, v2
	s_addc_u32 s16, s4, s15
	s_lshr_b32 s3, s15, 3
	v_lshrrev_b32_e32 v180, 4, v2
	s_and_b32 s2, s15, 7
	s_add_i32 s4, s3, 0xffffff28
	v_bitop3_b32 v2, v180, v2, 32 bitop3:0x6c
	s_cmpk_lt_u32 s15, 0x6c0
	v_ashrrev_i32_e32 v182, 31, v2
	s_cselect_b32 s3, s3, s4
	s_cmpk_gt_u32 s15, 0x6bf
	v_lshrrev_b32_e32 v182, 26, v182
	s_cselect_b32 s4, 8, 0
	s_and_b32 s5, s3, 7
	v_add_u32_e32 v182, v2, v182
	s_or_b32 s4, s5, s4
	v_lshrrev_b32_e32 v183, 6, v182
	v_and_b32_e32 v182, 0xc0, v182
	s_lshr_b32 s82, s3, 3
	s_lshl_b32 s3, s4, 3
	v_ashrrev_i32_e32 v181, 6, v181
	v_sub_u32_e32 v2, v2, v182
	s_or_b32 s14, s3, s2
	v_lshlrev_b32_e32 v180, 3, v181
	v_lshlrev_b32_e32 v181, 5, v181
	v_ashrrev_i16_sdwa v2, v196, sext(v2) dst_sel:DWORD dst_unused:UNUSED_PAD src0_sel:DWORD src1_sel:BYTE_0
	s_lshl_b64 s[2:3], s[82:83], 18
	v_and_b32_e32 v180, 0x3ffff0, v180
	v_and_b32_e32 v181, 32, v181
	v_bfe_i32 v2, v2, 0, 16
	s_add_u32 s4, s19, s2
	s_addc_u32 s5, s22, s3
	s_lshl_b32 s2, s14, 18
	v_add_lshl_u32 v180, v183, v180, 10
	v_add_lshl_u32 v2, v181, v2, 1
	v_add3_u32 v180, v180, s2, v2
	v_add_u32_e32 v181, 0x10000, v180
	v_add_u32_e32 v182, 0x20000, v180
	v_add_u32_e32 v183, 0x30000, v180
	s_mov_b64 s[6:7], s[8:9]
	s_mov_b32 s15, s16
	s_mov_b32 s16, s82
	s_branch .LBB0_257

.LBB0_902:
	ds_read_b128 v[20:23], v186
	ds_read_b128 v[24:27], v186 offset:1024
	ds_read_b128 v[28:31], v186 offset:2048
	ds_read_b128 v[32:35], v186 offset:3072
	ds_read_b128 v[4:7], v187
	ds_read_b128 v[8:11], v187 offset:1024
	ds_read_b128 v[12:15], v187 offset:2048
	ds_read_b128 v[16:19], v187 offset:3072
	v_add_u32_e32 v165, 0xc000, v172
	s_add_u32 s2, s34, 0x80
	v_mov_b32_e32 v164, v176
	v_readfirstlane_b32 s13, v165
	v_add_u32_e32 v165, 0xe000, v172
	ds_read_b128 v[204:207], v188
	ds_read_b128 v[208:211], v188 offset:1024
	ds_read_b128 v[212:215], v189
	ds_read_b128 v[216:219], v189 offset:1024
	ds_read_b128 v[220:223], v190
	ds_read_b128 v[224:227], v190 offset:1024
	ds_read_b128 v[228:231], v191
	ds_read_b128 v[232:235], v191 offset:1024
	s_addc_u32 s3, s35, 0
	s_mov_b32 m0, s13
	v_readfirstlane_b32 s12, v165
	global_load_lds_dwordx4 v164, s[2:3]
	v_mov_b32_e32 v164, v178
	s_mov_b32 m0, s12
	s_nop 0
	global_load_lds_dwordx4 v164, s[2:3]
	s_waitcnt vmcnt(8)
	s_waitcnt lgkmcnt(0)
	s_barrier
	s_setprio 1
	v_mfma_scale_f32_16x16x128_f8f6f4 v[160:163], v[20:27], v[204:211], v[160:163], v166, v167 op_sel_hi:[0,0,0]
	v_mfma_scale_f32_16x16x128_f8f6f4 v[156:159], v[28:35], v[204:211], v[156:159], v166, v167 op_sel_hi:[0,0,0]
	v_mfma_scale_f32_16x16x128_f8f6f4 v[152:155], v[20:27], v[212:219], v[152:155], v166, v167 op_sel_hi:[0,0,0]
	v_mfma_scale_f32_16x16x128_f8f6f4 v[148:151], v[28:35], v[212:219], v[148:151], v166, v167 op_sel_hi:[0,0,0]
	v_mfma_scale_f32_16x16x128_f8f6f4 v[144:147], v[20:27], v[220:227], v[144:147], v166, v167 op_sel_hi:[0,0,0]
	v_mfma_scale_f32_16x16x128_f8f6f4 v[140:143], v[28:35], v[220:227], v[140:143], v166, v167 op_sel_hi:[0,0,0]
	v_mfma_scale_f32_16x16x128_f8f6f4 v[136:139], v[20:27], v[228:235], v[136:139], v166, v167 op_sel_hi:[0,0,0]
	v_mfma_scale_f32_16x16x128_f8f6f4 v[132:135], v[28:35], v[228:235], v[132:135], v166, v167 op_sel_hi:[0,0,0]
	v_mfma_scale_f32_16x16x128_f8f6f4 v[128:131], v[4:11], v[204:211], v[128:131], v166, v167 op_sel_hi:[0,0,0]
	v_mfma_scale_f32_16x16x128_f8f6f4 v[124:127], v[12:19], v[204:211], v[124:127], v166, v167 op_sel_hi:[0,0,0]
	v_mfma_scale_f32_16x16x128_f8f6f4 v[120:123], v[4:11], v[212:219], v[120:123], v166, v167 op_sel_hi:[0,0,0]
	v_mfma_scale_f32_16x16x128_f8f6f4 v[116:119], v[12:19], v[212:219], v[116:119], v166, v167 op_sel_hi:[0,0,0]
	v_mfma_scale_f32_16x16x128_f8f6f4 v[112:115], v[4:11], v[220:227], v[112:115], v166, v167 op_sel_hi:[0,0,0]
	v_mfma_scale_f32_16x16x128_f8f6f4 v[108:111], v[12:19], v[220:227], v[108:111], v166, v167 op_sel_hi:[0,0,0]
	v_mfma_scale_f32_16x16x128_f8f6f4 v[104:107], v[4:11], v[228:235], v[104:107], v166, v167 op_sel_hi:[0,0,0]
	v_mfma_scale_f32_16x16x128_f8f6f4 v[100:103], v[12:19], v[228:235], v[100:103], v166, v167 op_sel_hi:[0,0,0]
	s_barrier
	s_setprio 0
	s_add_u32 s2, s6, 0x100
	v_mov_b32_e32 v164, v2
	v_readfirstlane_b32 s23, v168
	ds_read_b128 v[204:207], v188 offset:16384
	ds_read_b128 v[208:211], v188 offset:17408
	ds_read_b128 v[212:215], v189 offset:16384
	ds_read_b128 v[216:219], v189 offset:17408
	ds_read_b128 v[220:223], v190 offset:16384
	ds_read_b128 v[224:227], v190 offset:17408
	ds_read_b128 v[228:231], v191 offset:16384
	ds_read_b128 v[232:235], v191 offset:17408
	s_addc_u32 s3, s7, 0
	s_mov_b32 m0, s23
	v_readfirstlane_b32 s23, v169
	global_load_lds_dwordx4 v164, s[2:3]
	s_add_u32 s2, s6, 0x8100
	v_mov_b32_e32 v164, v2
	s_addc_u32 s3, s7, 0
	s_mov_b32 m0, s23
	v_readfirstlane_b32 s23, v170
	global_load_lds_dwordx4 v164, s[2:3]
	s_add_u32 s2, s6, 0x10100
	v_mov_b32_e32 v164, v2
	s_addc_u32 s3, s7, 0
	s_mov_b32 m0, s23
	v_readfirstlane_b32 s23, v171
	global_load_lds_dwordx4 v164, s[2:3]
	s_add_u32 s2, s6, 0x18100
	v_mov_b32_e32 v164, v2
	s_addc_u32 s3, s7, 0
	s_mov_b32 m0, s23
	v_readfirstlane_b32 s23, v172
	global_load_lds_dwordx4 v164, s[2:3]
	s_add_u32 s2, s34, 0x100
	v_mov_b32_e32 v164, v173
	s_addc_u32 s3, s35, 0
	s_mov_b32 m0, s23
	v_readfirstlane_b32 s23, v174
	global_load_lds_dwordx4 v164, s[2:3]
	v_mov_b32_e32 v164, v175
	s_mov_b32 m0, s23
	s_nop 0
	global_load_lds_dwordx4 v164, s[2:3]
	s_waitcnt vmcnt(8)
	s_waitcnt lgkmcnt(0)
	s_barrier
	s_setprio 1
	v_mfma_scale_f32_16x16x128_f8f6f4 v[96:99], v[20:27], v[204:211], v[96:99], v166, v167 op_sel_hi:[0,0,0]
	v_mfma_scale_f32_16x16x128_f8f6f4 v[92:95], v[28:35], v[204:211], v[92:95], v166, v167 op_sel_hi:[0,0,0]
	v_mfma_scale_f32_16x16x128_f8f6f4 v[88:91], v[20:27], v[212:219], v[88:91], v166, v167 op_sel_hi:[0,0,0]
	v_mfma_scale_f32_16x16x128_f8f6f4 v[84:87], v[28:35], v[212:219], v[84:87], v166, v167 op_sel_hi:[0,0,0]
	v_mfma_scale_f32_16x16x128_f8f6f4 v[80:83], v[20:27], v[220:227], v[80:83], v166, v167 op_sel_hi:[0,0,0]
	v_mfma_scale_f32_16x16x128_f8f6f4 v[76:79], v[28:35], v[220:227], v[76:79], v166, v167 op_sel_hi:[0,0,0]
	v_mfma_scale_f32_16x16x128_f8f6f4 v[72:75], v[20:27], v[228:235], v[72:75], v166, v167 op_sel_hi:[0,0,0]
	v_mfma_scale_f32_16x16x128_f8f6f4 v[68:71], v[28:35], v[228:235], v[68:71], v166, v167 op_sel_hi:[0,0,0]
	v_mfma_scale_f32_16x16x128_f8f6f4 v[64:67], v[4:11], v[204:211], v[64:67], v166, v167 op_sel_hi:[0,0,0]
	v_mfma_scale_f32_16x16x128_f8f6f4 v[60:63], v[12:19], v[204:211], v[60:63], v166, v167 op_sel_hi:[0,0,0]
	v_mfma_scale_f32_16x16x128_f8f6f4 v[56:59], v[4:11], v[212:219], v[56:59], v166, v167 op_sel_hi:[0,0,0]
	v_mfma_scale_f32_16x16x128_f8f6f4 v[52:55], v[12:19], v[212:219], v[52:55], v166, v167 op_sel_hi:[0,0,0]
	v_mfma_scale_f32_16x16x128_f8f6f4 v[48:51], v[4:11], v[220:227], v[48:51], v166, v167 op_sel_hi:[0,0,0]
	v_mfma_scale_f32_16x16x128_f8f6f4 v[44:47], v[12:19], v[220:227], v[44:47], v166, v167 op_sel_hi:[0,0,0]
	v_mfma_scale_f32_16x16x128_f8f6f4 v[40:43], v[4:11], v[228:235], v[40:43], v166, v167 op_sel_hi:[0,0,0]
	v_mfma_scale_f32_16x16x128_f8f6f4 v[36:39], v[12:19], v[228:235], v[36:39], v166, v167 op_sel_hi:[0,0,0]
	s_barrier
	s_setprio 0
	ds_read_b128 v[20:23], v201
	ds_read_b128 v[24:27], v201 offset:1024
	ds_read_b128 v[28:31], v201 offset:2048
	ds_read_b128 v[32:35], v201 offset:3072
	ds_read_b128 v[4:7], v202
	ds_read_b128 v[8:11], v202 offset:1024
	ds_read_b128 v[12:15], v202 offset:2048
	ds_read_b128 v[16:19], v202 offset:3072
	v_mov_b32_e32 v164, v176
	v_readfirstlane_b32 s23, v177
	ds_read_b128 v[204:207], v188 offset:32768
	ds_read_b128 v[208:211], v188 offset:33792
	ds_read_b128 v[212:215], v189 offset:32768
	ds_read_b128 v[216:219], v189 offset:33792
	ds_read_b128 v[220:223], v190 offset:32768
	ds_read_b128 v[224:227], v190 offset:33792
	ds_read_b128 v[228:231], v191 offset:32768
	ds_read_b128 v[232:235], v191 offset:33792
	s_mov_b32 m0, s23
	v_readfirstlane_b32 s23, v179
	global_load_lds_dwordx4 v164, s[2:3]
	v_mov_b32_e32 v164, v178
	s_mov_b32 m0, s23
	s_nop 0
	global_load_lds_dwordx4 v164, s[2:3]
	s_waitcnt vmcnt(8)
	s_waitcnt lgkmcnt(0)
	s_barrier
	s_setprio 1
	v_mfma_scale_f32_16x16x128_f8f6f4 v[160:163], v[20:27], v[204:211], v[160:163], v166, v167 op_sel_hi:[0,0,0]
	v_mfma_scale_f32_16x16x128_f8f6f4 v[156:159], v[28:35], v[204:211], v[156:159], v166, v167 op_sel_hi:[0,0,0]
	v_mfma_scale_f32_16x16x128_f8f6f4 v[152:155], v[20:27], v[212:219], v[152:155], v166, v167 op_sel_hi:[0,0,0]
	v_mfma_scale_f32_16x16x128_f8f6f4 v[148:151], v[28:35], v[212:219], v[148:151], v166, v167 op_sel_hi:[0,0,0]
	v_mfma_scale_f32_16x16x128_f8f6f4 v[144:147], v[20:27], v[220:227], v[144:147], v166, v167 op_sel_hi:[0,0,0]
	v_mfma_scale_f32_16x16x128_f8f6f4 v[140:143], v[28:35], v[220:227], v[140:143], v166, v167 op_sel_hi:[0,0,0]
	v_mfma_scale_f32_16x16x128_f8f6f4 v[136:139], v[20:27], v[228:235], v[136:139], v166, v167 op_sel_hi:[0,0,0]
	v_mfma_scale_f32_16x16x128_f8f6f4 v[132:135], v[28:35], v[228:235], v[132:135], v166, v167 op_sel_hi:[0,0,0]
	v_mfma_scale_f32_16x16x128_f8f6f4 v[128:131], v[4:11], v[204:211], v[128:131], v166, v167 op_sel_hi:[0,0,0]
	v_mfma_scale_f32_16x16x128_f8f6f4 v[124:127], v[12:19], v[204:211], v[124:127], v166, v167 op_sel_hi:[0,0,0]
	v_mfma_scale_f32_16x16x128_f8f6f4 v[120:123], v[4:11], v[212:219], v[120:123], v166, v167 op_sel_hi:[0,0,0]
	v_mfma_scale_f32_16x16x128_f8f6f4 v[116:119], v[12:19], v[212:219], v[116:119], v166, v167 op_sel_hi:[0,0,0]
	v_mfma_scale_f32_16x16x128_f8f6f4 v[112:115], v[4:11], v[220:227], v[112:115], v166, v167 op_sel_hi:[0,0,0]
	v_mfma_scale_f32_16x16x128_f8f6f4 v[108:111], v[12:19], v[220:227], v[108:111], v166, v167 op_sel_hi:[0,0,0]
	v_mfma_scale_f32_16x16x128_f8f6f4 v[104:107], v[4:11], v[228:235], v[104:107], v166, v167 op_sel_hi:[0,0,0]
	v_mfma_scale_f32_16x16x128_f8f6f4 v[100:103], v[12:19], v[228:235], v[100:103], v166, v167 op_sel_hi:[0,0,0]
	s_barrier
	s_setprio 0
	s_add_u32 s2, s6, 0x180
	v_mov_b32_e32 v164, v2
	v_readfirstlane_b32 s23, v180
	ds_read_b128 v[204:207], v188 offset:49152
	ds_read_b128 v[208:211], v188 offset:50176
	ds_read_b128 v[212:215], v189 offset:49152
	ds_read_b128 v[216:219], v189 offset:50176
	ds_read_b128 v[220:223], v190 offset:49152
	ds_read_b128 v[224:227], v190 offset:50176
	ds_read_b128 v[228:231], v191 offset:49152
	ds_read_b128 v[232:235], v191 offset:50176
	s_addc_u32 s3, s7, 0
	s_mov_b32 m0, s23
	v_readfirstlane_b32 s23, v181
	global_load_lds_dwordx4 v164, s[2:3]
	s_add_u32 s2, s6, 0x8180
	v_mov_b32_e32 v164, v2
	s_addc_u32 s3, s7, 0
	s_mov_b32 m0, s23
	v_readfirstlane_b32 s23, v184
	global_load_lds_dwordx4 v164, s[2:3]
	s_add_u32 s2, s6, 0x10180
	v_mov_b32_e32 v164, v2
	s_addc_u32 s3, s7, 0
	s_mov_b32 m0, s23
	v_readfirstlane_b32 s23, v185
	global_load_lds_dwordx4 v164, s[2:3]
	s_add_u32 s2, s6, 0x18180
	v_mov_b32_e32 v164, v2
	s_addc_u32 s3, s7, 0
	s_mov_b32 m0, s23
	v_readfirstlane_b32 s23, v182
	global_load_lds_dwordx4 v164, s[2:3]
	s_add_u32 s2, s34, 0x180
	v_mov_b32_e32 v164, v173
	s_addc_u32 s3, s35, 0
	s_mov_b32 m0, s23
	v_readfirstlane_b32 s23, v183
	global_load_lds_dwordx4 v164, s[2:3]
	v_mov_b32_e32 v164, v175
	s_mov_b32 m0, s23
	s_nop 0
	global_load_lds_dwordx4 v164, s[2:3]
	s_waitcnt vmcnt(8)
	s_waitcnt lgkmcnt(0)
	s_barrier
	s_setprio 1
	v_mfma_scale_f32_16x16x128_f8f6f4 v[96:99], v[20:27], v[204:211], v[96:99], v166, v167 op_sel_hi:[0,0,0]
	v_mfma_scale_f32_16x16x128_f8f6f4 v[92:95], v[28:35], v[204:211], v[92:95], v166, v167 op_sel_hi:[0,0,0]
	v_mfma_scale_f32_16x16x128_f8f6f4 v[88:91], v[20:27], v[212:219], v[88:91], v166, v167 op_sel_hi:[0,0,0]
	v_mfma_scale_f32_16x16x128_f8f6f4 v[84:87], v[28:35], v[212:219], v[84:87], v166, v167 op_sel_hi:[0,0,0]
	v_mfma_scale_f32_16x16x128_f8f6f4 v[80:83], v[20:27], v[220:227], v[80:83], v166, v167 op_sel_hi:[0,0,0]
	v_mfma_scale_f32_16x16x128_f8f6f4 v[76:79], v[28:35], v[220:227], v[76:79], v166, v167 op_sel_hi:[0,0,0]
	v_mfma_scale_f32_16x16x128_f8f6f4 v[72:75], v[20:27], v[228:235], v[72:75], v166, v167 op_sel_hi:[0,0,0]
	v_mfma_scale_f32_16x16x128_f8f6f4 v[68:71], v[28:35], v[228:235], v[68:71], v166, v167 op_sel_hi:[0,0,0]
	v_mfma_scale_f32_16x16x128_f8f6f4 v[64:67], v[4:11], v[204:211], v[64:67], v166, v167 op_sel_hi:[0,0,0]
	v_mfma_scale_f32_16x16x128_f8f6f4 v[60:63], v[12:19], v[204:211], v[60:63], v166, v167 op_sel_hi:[0,0,0]
	v_mfma_scale_f32_16x16x128_f8f6f4 v[56:59], v[4:11], v[212:219], v[56:59], v166, v167 op_sel_hi:[0,0,0]
	v_mfma_scale_f32_16x16x128_f8f6f4 v[52:55], v[12:19], v[212:219], v[52:55], v166, v167 op_sel_hi:[0,0,0]
	v_mfma_scale_f32_16x16x128_f8f6f4 v[48:51], v[4:11], v[220:227], v[48:51], v166, v167 op_sel_hi:[0,0,0]
	v_mfma_scale_f32_16x16x128_f8f6f4 v[44:47], v[12:19], v[220:227], v[44:47], v166, v167 op_sel_hi:[0,0,0]
	v_mfma_scale_f32_16x16x128_f8f6f4 v[40:43], v[4:11], v[228:235], v[40:43], v166, v167 op_sel_hi:[0,0,0]
	v_mfma_scale_f32_16x16x128_f8f6f4 v[36:39], v[12:19], v[228:235], v[36:39], v166, v167 op_sel_hi:[0,0,0]
	s_barrier
	s_setprio 0
	ds_read_b128 v[20:23], v186
	ds_read_b128 v[24:27], v186 offset:1024
	ds_read_b128 v[28:31], v186 offset:2048
	ds_read_b128 v[32:35], v186 offset:3072
	ds_read_b128 v[4:7], v187
	ds_read_b128 v[8:11], v187 offset:1024
	ds_read_b128 v[12:15], v187 offset:2048
	ds_read_b128 v[16:19], v187 offset:3072
	v_mov_b32_e32 v164, v176
	s_mov_b32 m0, s13
	ds_read_b128 v[204:207], v188
	ds_read_b128 v[208:211], v188 offset:1024
	ds_read_b128 v[212:215], v189
	ds_read_b128 v[216:219], v189 offset:1024
	ds_read_b128 v[220:223], v190
	ds_read_b128 v[224:227], v190 offset:1024
	ds_read_b128 v[228:231], v191
	ds_read_b128 v[232:235], v191 offset:1024
	s_nop 0
	global_load_lds_dwordx4 v164, s[2:3]
	v_mov_b32_e32 v164, v178
	s_mov_b32 m0, s12
	s_nop 0
	global_load_lds_dwordx4 v164, s[2:3]
	s_waitcnt vmcnt(8)
	s_waitcnt lgkmcnt(0)
	s_barrier
	s_setprio 1
	v_mfma_scale_f32_16x16x128_f8f6f4 v[160:163], v[20:27], v[204:211], v[160:163], v166, v167 op_sel_hi:[0,0,0]
	v_mfma_scale_f32_16x16x128_f8f6f4 v[156:159], v[28:35], v[204:211], v[156:159], v166, v167 op_sel_hi:[0,0,0]
	v_mfma_scale_f32_16x16x128_f8f6f4 v[152:155], v[20:27], v[212:219], v[152:155], v166, v167 op_sel_hi:[0,0,0]
	v_mfma_scale_f32_16x16x128_f8f6f4 v[148:151], v[28:35], v[212:219], v[148:151], v166, v167 op_sel_hi:[0,0,0]
	v_mfma_scale_f32_16x16x128_f8f6f4 v[144:147], v[20:27], v[220:227], v[144:147], v166, v167 op_sel_hi:[0,0,0]
	v_mfma_scale_f32_16x16x128_f8f6f4 v[140:143], v[28:35], v[220:227], v[140:143], v166, v167 op_sel_hi:[0,0,0]
	v_mfma_scale_f32_16x16x128_f8f6f4 v[136:139], v[20:27], v[228:235], v[136:139], v166, v167 op_sel_hi:[0,0,0]
	v_mfma_scale_f32_16x16x128_f8f6f4 v[132:135], v[28:35], v[228:235], v[132:135], v166, v167 op_sel_hi:[0,0,0]
	v_mfma_scale_f32_16x16x128_f8f6f4 v[128:131], v[4:11], v[204:211], v[128:131], v166, v167 op_sel_hi:[0,0,0]
	v_mfma_scale_f32_16x16x128_f8f6f4 v[124:127], v[12:19], v[204:211], v[124:127], v166, v167 op_sel_hi:[0,0,0]
	v_mfma_scale_f32_16x16x128_f8f6f4 v[120:123], v[4:11], v[212:219], v[120:123], v166, v167 op_sel_hi:[0,0,0]
	v_mfma_scale_f32_16x16x128_f8f6f4 v[116:119], v[12:19], v[212:219], v[116:119], v166, v167 op_sel_hi:[0,0,0]
	v_mfma_scale_f32_16x16x128_f8f6f4 v[112:115], v[4:11], v[220:227], v[112:115], v166, v167 op_sel_hi:[0,0,0]
	v_mfma_scale_f32_16x16x128_f8f6f4 v[108:111], v[12:19], v[220:227], v[108:111], v166, v167 op_sel_hi:[0,0,0]
	v_mfma_scale_f32_16x16x128_f8f6f4 v[104:107], v[4:11], v[228:235], v[104:107], v166, v167 op_sel_hi:[0,0,0]
	v_mfma_scale_f32_16x16x128_f8f6f4 v[100:103], v[12:19], v[228:235], v[100:103], v166, v167 op_sel_hi:[0,0,0]
	s_barrier
	s_setprio 0
	s_cmp_gt_i32 s22, 1
	s_cselect_b64 s[40:41], -1, 0
	s_cmp_lt_i32 s22, 2
	s_cbranch_scc1 .LBB0_907
	s_mov_b64 s[12:13], 0
	s_cmpk_lt_u32 s21, 0x200
	s_mov_b32 s23, s21
	s_mov_b64 s[2:3], 0
	s_cbranch_scc0 .LBB0_905
	s_lshr_b32 s3, s21, 3
	s_add_i32 s23, s18, s21
	s_and_b32 s2, s21, 7
	s_sub_i32 s19, s3, 32
	s_cmpk_lt_u32 s21, 0x100
	s_cselect_b32 s3, s3, s19
	s_lshr_b32 s19, s21, 5
	s_and_b32 s19, s19, 8
	s_and_b32 s24, s3, 7
	s_or_b32 s19, s24, s19
	s_lshr_b32 s24, s3, 3
	s_lshl_b32 s3, s19, 3
	s_or_b32 s19, s3, s2
	s_mov_b64 s[2:3], -1
	s_mov_b32 s82, 0
	s_and_b64 vcc, exec, s[12:13]
	s_cbranch_vccz .LBB0_908
	s_branch .LBB0_906

.LBB0_910:
	v_mov_b32_e32 v164, v2
	v_readfirstlane_b32 s2, v168
	ds_read_b128 v[204:207], v188 offset:16384
	ds_read_b128 v[208:211], v188 offset:17408
	ds_read_b128 v[212:215], v189 offset:16384
	ds_read_b128 v[216:219], v189 offset:17408
	ds_read_b128 v[220:223], v190 offset:16384
	ds_read_b128 v[224:227], v190 offset:17408
	ds_read_b128 v[228:231], v191 offset:16384
	ds_read_b128 v[232:235], v191 offset:17408
	s_mov_b32 m0, s2
	s_add_u32 s2, s6, 0x8000
	global_load_lds_dwordx4 v164, s[6:7]
	v_mov_b32_e32 v164, v2
	v_readfirstlane_b32 s21, v169
	s_addc_u32 s3, s7, 0
	s_mov_b32 m0, s21
	v_readfirstlane_b32 s21, v170
	global_load_lds_dwordx4 v164, s[2:3]
	s_add_u32 s2, s6, 0x10000
	v_mov_b32_e32 v164, v2
	s_addc_u32 s3, s7, 0
	s_mov_b32 m0, s21
	v_readfirstlane_b32 s21, v171
	global_load_lds_dwordx4 v164, s[2:3]
	s_add_u32 s2, s6, 0x18000
	v_mov_b32_e32 v164, v2
	s_addc_u32 s3, s7, 0
	s_mov_b32 m0, s21
	s_nop 0
	global_load_lds_dwordx4 v164, s[2:3]
	v_mov_b32_e32 v164, v173
	v_readfirstlane_b32 s2, v172
	s_mov_b32 m0, s2
	v_readfirstlane_b32 s2, v174
	global_load_lds_dwordx4 v164, s[34:35]
	v_mov_b32_e32 v164, v175
	s_mov_b32 m0, s2
	s_nop 0
	global_load_lds_dwordx4 v164, s[34:35]
	s_waitcnt vmcnt(8)
	s_waitcnt lgkmcnt(0)
	s_barrier
	s_setprio 1
	v_mfma_scale_f32_16x16x128_f8f6f4 v[96:99], v[20:27], v[204:211], v[96:99], v166, v167 op_sel_hi:[0,0,0]
	v_mfma_scale_f32_16x16x128_f8f6f4 v[92:95], v[28:35], v[204:211], v[92:95], v166, v167 op_sel_hi:[0,0,0]
	v_mfma_scale_f32_16x16x128_f8f6f4 v[88:91], v[20:27], v[212:219], v[88:91], v166, v167 op_sel_hi:[0,0,0]
	v_mfma_scale_f32_16x16x128_f8f6f4 v[84:87], v[28:35], v[212:219], v[84:87], v166, v167 op_sel_hi:[0,0,0]
	v_mfma_scale_f32_16x16x128_f8f6f4 v[80:83], v[20:27], v[220:227], v[80:83], v166, v167 op_sel_hi:[0,0,0]
	v_mfma_scale_f32_16x16x128_f8f6f4 v[76:79], v[28:35], v[220:227], v[76:79], v166, v167 op_sel_hi:[0,0,0]
	v_mfma_scale_f32_16x16x128_f8f6f4 v[72:75], v[20:27], v[228:235], v[72:75], v166, v167 op_sel_hi:[0,0,0]
	v_mfma_scale_f32_16x16x128_f8f6f4 v[68:71], v[28:35], v[228:235], v[68:71], v166, v167 op_sel_hi:[0,0,0]
	v_mfma_scale_f32_16x16x128_f8f6f4 v[64:67], v[4:11], v[204:211], v[64:67], v166, v167 op_sel_hi:[0,0,0]
	v_mfma_scale_f32_16x16x128_f8f6f4 v[60:63], v[12:19], v[204:211], v[60:63], v166, v167 op_sel_hi:[0,0,0]
	v_mfma_scale_f32_16x16x128_f8f6f4 v[56:59], v[4:11], v[212:219], v[56:59], v166, v167 op_sel_hi:[0,0,0]
	v_mfma_scale_f32_16x16x128_f8f6f4 v[52:55], v[12:19], v[212:219], v[52:55], v166, v167 op_sel_hi:[0,0,0]
	v_mfma_scale_f32_16x16x128_f8f6f4 v[48:51], v[4:11], v[220:227], v[48:51], v166, v167 op_sel_hi:[0,0,0]
	v_mfma_scale_f32_16x16x128_f8f6f4 v[44:47], v[12:19], v[220:227], v[44:47], v166, v167 op_sel_hi:[0,0,0]
	v_mfma_scale_f32_16x16x128_f8f6f4 v[40:43], v[4:11], v[228:235], v[40:43], v166, v167 op_sel_hi:[0,0,0]
	v_mfma_scale_f32_16x16x128_f8f6f4 v[36:39], v[12:19], v[228:235], v[36:39], v166, v167 op_sel_hi:[0,0,0]
	s_barrier
	s_setprio 0
	ds_read_b128 v[20:23], v201
	ds_read_b128 v[24:27], v201 offset:1024
	ds_read_b128 v[28:31], v201 offset:2048
	ds_read_b128 v[32:35], v201 offset:3072
	ds_read_b128 v[4:7], v202
	ds_read_b128 v[8:11], v202 offset:1024
	ds_read_b128 v[12:15], v202 offset:2048
	ds_read_b128 v[16:19], v202 offset:3072
	v_mov_b32_e32 v164, v176
	v_readfirstlane_b32 s2, v177
	ds_read_b128 v[204:207], v188 offset:32768
	ds_read_b128 v[208:211], v188 offset:33792
	ds_read_b128 v[212:215], v189 offset:32768
	ds_read_b128 v[216:219], v189 offset:33792
	ds_read_b128 v[220:223], v190 offset:32768
	ds_read_b128 v[224:227], v190 offset:33792
	ds_read_b128 v[228:231], v191 offset:32768
	ds_read_b128 v[232:235], v191 offset:33792
	s_mov_b32 m0, s2
	v_readfirstlane_b32 s2, v179
	global_load_lds_dwordx4 v164, s[34:35]
	v_mov_b32_e32 v164, v178
	s_mov_b32 m0, s2
	s_nop 0
	global_load_lds_dwordx4 v164, s[34:35]
	s_waitcnt vmcnt(8)
	s_waitcnt lgkmcnt(0)
	s_barrier
	s_setprio 1
	v_mfma_scale_f32_16x16x128_f8f6f4 v[160:163], v[20:27], v[204:211], v[160:163], v166, v167 op_sel_hi:[0,0,0]
	v_mfma_scale_f32_16x16x128_f8f6f4 v[156:159], v[28:35], v[204:211], v[156:159], v166, v167 op_sel_hi:[0,0,0]
	v_mfma_scale_f32_16x16x128_f8f6f4 v[152:155], v[20:27], v[212:219], v[152:155], v166, v167 op_sel_hi:[0,0,0]
	v_mfma_scale_f32_16x16x128_f8f6f4 v[148:151], v[28:35], v[212:219], v[148:151], v166, v167 op_sel_hi:[0,0,0]
	v_mfma_scale_f32_16x16x128_f8f6f4 v[144:147], v[20:27], v[220:227], v[144:147], v166, v167 op_sel_hi:[0,0,0]
	v_mfma_scale_f32_16x16x128_f8f6f4 v[140:143], v[28:35], v[220:227], v[140:143], v166, v167 op_sel_hi:[0,0,0]
	v_mfma_scale_f32_16x16x128_f8f6f4 v[136:139], v[20:27], v[228:235], v[136:139], v166, v167 op_sel_hi:[0,0,0]
	v_mfma_scale_f32_16x16x128_f8f6f4 v[132:135], v[28:35], v[228:235], v[132:135], v166, v167 op_sel_hi:[0,0,0]
	v_mfma_scale_f32_16x16x128_f8f6f4 v[128:131], v[4:11], v[204:211], v[128:131], v166, v167 op_sel_hi:[0,0,0]
	v_mfma_scale_f32_16x16x128_f8f6f4 v[124:127], v[12:19], v[204:211], v[124:127], v166, v167 op_sel_hi:[0,0,0]
	v_mfma_scale_f32_16x16x128_f8f6f4 v[120:123], v[4:11], v[212:219], v[120:123], v166, v167 op_sel_hi:[0,0,0]
	v_mfma_scale_f32_16x16x128_f8f6f4 v[116:119], v[12:19], v[212:219], v[116:119], v166, v167 op_sel_hi:[0,0,0]
	v_mfma_scale_f32_16x16x128_f8f6f4 v[112:115], v[4:11], v[220:227], v[112:115], v166, v167 op_sel_hi:[0,0,0]
	v_mfma_scale_f32_16x16x128_f8f6f4 v[108:111], v[12:19], v[220:227], v[108:111], v166, v167 op_sel_hi:[0,0,0]
	v_mfma_scale_f32_16x16x128_f8f6f4 v[104:107], v[4:11], v[228:235], v[104:107], v166, v167 op_sel_hi:[0,0,0]
	v_mfma_scale_f32_16x16x128_f8f6f4 v[100:103], v[12:19], v[228:235], v[100:103], v166, v167 op_sel_hi:[0,0,0]
	s_barrier
	s_setprio 0
	s_add_u32 s2, s6, 0x80
	v_mov_b32_e32 v164, v2
	v_readfirstlane_b32 s21, v180
	ds_read_b128 v[204:207], v188 offset:49152
	ds_read_b128 v[208:211], v188 offset:50176
	ds_read_b128 v[212:215], v189 offset:49152
	ds_read_b128 v[216:219], v189 offset:50176
	ds_read_b128 v[220:223], v190 offset:49152
	ds_read_b128 v[224:227], v190 offset:50176
	ds_read_b128 v[228:231], v191 offset:49152
	ds_read_b128 v[232:235], v191 offset:50176
	s_addc_u32 s3, s7, 0
	s_mov_b32 m0, s21
	v_readfirstlane_b32 s21, v181
	global_load_lds_dwordx4 v164, s[2:3]
	s_add_u32 s2, s6, 0x8080
	v_mov_b32_e32 v164, v2
	s_addc_u32 s3, s7, 0
	s_mov_b32 m0, s21
	v_readfirstlane_b32 s21, v184
	global_load_lds_dwordx4 v164, s[2:3]
	s_add_u32 s2, s6, 0x10080
	v_mov_b32_e32 v164, v2
	s_addc_u32 s3, s7, 0
	s_mov_b32 m0, s21
	v_readfirstlane_b32 s21, v185
	global_load_lds_dwordx4 v164, s[2:3]
	s_add_u32 s2, s6, 0x18080
	v_mov_b32_e32 v164, v2
	s_addc_u32 s3, s7, 0
	s_mov_b32 m0, s21
	v_readfirstlane_b32 s21, v182
	global_load_lds_dwordx4 v164, s[2:3]
	s_add_u32 s2, s34, 0x80
	v_mov_b32_e32 v164, v173
	s_addc_u32 s3, s35, 0
	s_mov_b32 m0, s21
	v_readfirstlane_b32 s21, v183
	global_load_lds_dwordx4 v164, s[2:3]
	v_mov_b32_e32 v164, v175
	s_mov_b32 m0, s21
	s_nop 0
	global_load_lds_dwordx4 v164, s[2:3]
	s_waitcnt vmcnt(8)
	s_waitcnt lgkmcnt(0)
	s_barrier
	s_setprio 1
	v_mfma_scale_f32_16x16x128_f8f6f4 v[96:99], v[20:27], v[204:211], v[96:99], v166, v167 op_sel_hi:[0,0,0]
	v_mfma_scale_f32_16x16x128_f8f6f4 v[92:95], v[28:35], v[204:211], v[92:95], v166, v167 op_sel_hi:[0,0,0]
	v_mfma_scale_f32_16x16x128_f8f6f4 v[88:91], v[20:27], v[212:219], v[88:91], v166, v167 op_sel_hi:[0,0,0]
	v_mfma_scale_f32_16x16x128_f8f6f4 v[84:87], v[28:35], v[212:219], v[84:87], v166, v167 op_sel_hi:[0,0,0]
	v_mfma_scale_f32_16x16x128_f8f6f4 v[80:83], v[20:27], v[220:227], v[80:83], v166, v167 op_sel_hi:[0,0,0]
	v_mfma_scale_f32_16x16x128_f8f6f4 v[76:79], v[28:35], v[220:227], v[76:79], v166, v167 op_sel_hi:[0,0,0]
	v_mfma_scale_f32_16x16x128_f8f6f4 v[72:75], v[20:27], v[228:235], v[72:75], v166, v167 op_sel_hi:[0,0,0]
	v_mfma_scale_f32_16x16x128_f8f6f4 v[68:71], v[28:35], v[228:235], v[68:71], v166, v167 op_sel_hi:[0,0,0]
	v_mfma_scale_f32_16x16x128_f8f6f4 v[64:67], v[4:11], v[204:211], v[64:67], v166, v167 op_sel_hi:[0,0,0]
	v_mfma_scale_f32_16x16x128_f8f6f4 v[60:63], v[12:19], v[204:211], v[60:63], v166, v167 op_sel_hi:[0,0,0]
	v_mfma_scale_f32_16x16x128_f8f6f4 v[56:59], v[4:11], v[212:219], v[56:59], v166, v167 op_sel_hi:[0,0,0]
	v_mfma_scale_f32_16x16x128_f8f6f4 v[52:55], v[12:19], v[212:219], v[52:55], v166, v167 op_sel_hi:[0,0,0]
	v_mfma_scale_f32_16x16x128_f8f6f4 v[48:51], v[4:11], v[220:227], v[48:51], v166, v167 op_sel_hi:[0,0,0]
	v_mfma_scale_f32_16x16x128_f8f6f4 v[44:47], v[12:19], v[220:227], v[44:47], v166, v167 op_sel_hi:[0,0,0]
	v_mfma_scale_f32_16x16x128_f8f6f4 v[40:43], v[4:11], v[228:235], v[40:43], v166, v167 op_sel_hi:[0,0,0]
	v_mfma_scale_f32_16x16x128_f8f6f4 v[36:39], v[12:19], v[228:235], v[36:39], v166, v167 op_sel_hi:[0,0,0]
	s_barrier
	s_setprio 0
	s_and_saveexec_b64 s[2:3], s[38:39]
	s_cbranch_execz .LBB0_912
	s_barrier

.LBB0_1008:
	s_lshl_b64 s[2:3], s[82:83], 7
	s_add_u32 s26, s10, s2
	v_mov_b32_e32 v2, v201
	v_readfirstlane_b32 s28, v204
	ds_read_b128 v[180:183], v226 offset:16384
	ds_read_b128 v[184:187], v226 offset:17408
	ds_read_b128 v[188:191], v227 offset:16384
	ds_read_b128 v[192:195], v227 offset:17408
	ds_read_b128 v[230:233], v228 offset:16384
	ds_read_b128 v[234:237], v228 offset:17408
	ds_read_b128 v[238:241], v229 offset:16384
	ds_read_b128 v[242:245], v229 offset:17408
	s_addc_u32 s27, s11, s3
	s_mov_b32 m0, s28
	s_add_u32 s28, s26, 0x10000
	global_load_lds_dwordx4 v2, s[26:27]
	v_mov_b32_e32 v2, v201
	v_readfirstlane_b32 s30, v205
	s_addc_u32 s29, s27, 0
	s_mov_b32 m0, s30
	v_readfirstlane_b32 s30, v206
	global_load_lds_dwordx4 v2, s[28:29]
	s_add_u32 s28, s26, 0x20000
	v_mov_b32_e32 v2, v201
	s_addc_u32 s29, s27, 0
	s_mov_b32 m0, s30
	s_add_u32 s26, s26, 0x30000
	global_load_lds_dwordx4 v2, s[28:29]
	v_mov_b32_e32 v2, v201
	v_readfirstlane_b32 s28, v207
	s_addc_u32 s27, s27, 0
	s_mov_b32 m0, s28
	s_add_u32 s2, s8, s2
	global_load_lds_dwordx4 v2, s[26:27]
	v_mov_b32_e32 v2, v209
	v_readfirstlane_b32 s26, v208
	s_addc_u32 s3, s9, s3
	s_mov_b32 m0, s26
	v_readfirstlane_b32 s26, v213
	global_load_lds_dwordx4 v2, s[2:3]
	v_mov_b32_e32 v2, v210
	s_mov_b32 m0, s26
	s_nop 0
	global_load_lds_dwordx4 v2, s[2:3]
	s_waitcnt vmcnt(8)
	s_waitcnt lgkmcnt(0)
	s_barrier
	s_setprio 1
	v_mfma_scale_f32_16x16x128_f8f6f4 v[112:115], v[20:27], v[180:187], v[112:115], v202, v203 op_sel_hi:[0,0,0]
	v_mfma_scale_f32_16x16x128_f8f6f4 v[108:111], v[28:35], v[180:187], v[108:111], v202, v203 op_sel_hi:[0,0,0]
	v_mfma_scale_f32_16x16x128_f8f6f4 v[104:107], v[20:27], v[188:195], v[104:107], v202, v203 op_sel_hi:[0,0,0]
	v_mfma_scale_f32_16x16x128_f8f6f4 v[100:103], v[28:35], v[188:195], v[100:103], v202, v203 op_sel_hi:[0,0,0]
	v_mfma_scale_f32_16x16x128_f8f6f4 v[96:99], v[20:27], v[230:237], v[96:99], v202, v203 op_sel_hi:[0,0,0]
	v_mfma_scale_f32_16x16x128_f8f6f4 v[92:95], v[28:35], v[230:237], v[92:95], v202, v203 op_sel_hi:[0,0,0]
	v_mfma_scale_f32_16x16x128_f8f6f4 v[88:91], v[20:27], v[238:245], v[88:91], v202, v203 op_sel_hi:[0,0,0]
	v_mfma_scale_f32_16x16x128_f8f6f4 v[84:87], v[28:35], v[238:245], v[84:87], v202, v203 op_sel_hi:[0,0,0]
	v_mfma_scale_f32_16x16x128_f8f6f4 v[80:83], v[4:11], v[180:187], v[80:83], v202, v203 op_sel_hi:[0,0,0]
	v_mfma_scale_f32_16x16x128_f8f6f4 v[76:79], v[12:19], v[180:187], v[76:79], v202, v203 op_sel_hi:[0,0,0]
	v_mfma_scale_f32_16x16x128_f8f6f4 v[72:75], v[4:11], v[188:195], v[72:75], v202, v203 op_sel_hi:[0,0,0]
	v_mfma_scale_f32_16x16x128_f8f6f4 v[68:71], v[12:19], v[188:195], v[68:71], v202, v203 op_sel_hi:[0,0,0]
	v_mfma_scale_f32_16x16x128_f8f6f4 v[64:67], v[4:11], v[230:237], v[64:67], v202, v203 op_sel_hi:[0,0,0]
	v_mfma_scale_f32_16x16x128_f8f6f4 v[60:63], v[12:19], v[230:237], v[60:63], v202, v203 op_sel_hi:[0,0,0]
	v_mfma_scale_f32_16x16x128_f8f6f4 v[56:59], v[4:11], v[238:245], v[56:59], v202, v203 op_sel_hi:[0,0,0]
	v_mfma_scale_f32_16x16x128_f8f6f4 v[52:55], v[12:19], v[238:245], v[52:55], v202, v203 op_sel_hi:[0,0,0]
	s_barrier
	s_setprio 0
	ds_read_b128 v[20:23], v224
	ds_read_b128 v[24:27], v224 offset:1024
	ds_read_b128 v[28:31], v224 offset:2048
	ds_read_b128 v[32:35], v224 offset:3072
	ds_read_b128 v[4:7], v225
	ds_read_b128 v[8:11], v225 offset:1024
	ds_read_b128 v[12:15], v225 offset:2048
	ds_read_b128 v[16:19], v225 offset:3072
	v_mov_b32_e32 v2, v211
	v_readfirstlane_b32 s26, v214
	ds_read_b128 v[180:183], v226 offset:32768
	ds_read_b128 v[184:187], v226 offset:33792
	ds_read_b128 v[188:191], v227 offset:32768
	ds_read_b128 v[192:195], v227 offset:33792
	ds_read_b128 v[230:233], v228 offset:32768
	ds_read_b128 v[234:237], v228 offset:33792
	ds_read_b128 v[238:241], v229 offset:32768
	ds_read_b128 v[242:245], v229 offset:33792
	s_mov_b32 m0, s26
	v_readfirstlane_b32 s26, v215
	global_load_lds_dwordx4 v2, s[2:3]
	v_mov_b32_e32 v2, v212
	s_mov_b32 m0, s26
	s_nop 0
	global_load_lds_dwordx4 v2, s[2:3]
	s_waitcnt vmcnt(8)
	s_waitcnt lgkmcnt(0)
	s_barrier
	s_setprio 1
	v_mfma_scale_f32_16x16x128_f8f6f4 v[176:179], v[20:27], v[180:187], v[176:179], v202, v203 op_sel_hi:[0,0,0]
	v_mfma_scale_f32_16x16x128_f8f6f4 v[172:175], v[28:35], v[180:187], v[172:175], v202, v203 op_sel_hi:[0,0,0]
	v_mfma_scale_f32_16x16x128_f8f6f4 v[168:171], v[20:27], v[188:195], v[168:171], v202, v203 op_sel_hi:[0,0,0]
	v_mfma_scale_f32_16x16x128_f8f6f4 v[164:167], v[28:35], v[188:195], v[164:167], v202, v203 op_sel_hi:[0,0,0]
	v_mfma_scale_f32_16x16x128_f8f6f4 v[160:163], v[20:27], v[230:237], v[160:163], v202, v203 op_sel_hi:[0,0,0]
	v_mfma_scale_f32_16x16x128_f8f6f4 v[156:159], v[28:35], v[230:237], v[156:159], v202, v203 op_sel_hi:[0,0,0]
	v_mfma_scale_f32_16x16x128_f8f6f4 v[152:155], v[20:27], v[238:245], v[152:155], v202, v203 op_sel_hi:[0,0,0]
	v_mfma_scale_f32_16x16x128_f8f6f4 v[148:151], v[28:35], v[238:245], v[148:151], v202, v203 op_sel_hi:[0,0,0]
	v_mfma_scale_f32_16x16x128_f8f6f4 v[144:147], v[4:11], v[180:187], v[144:147], v202, v203 op_sel_hi:[0,0,0]
	v_mfma_scale_f32_16x16x128_f8f6f4 v[140:143], v[12:19], v[180:187], v[140:143], v202, v203 op_sel_hi:[0,0,0]
	v_mfma_scale_f32_16x16x128_f8f6f4 v[136:139], v[4:11], v[188:195], v[136:139], v202, v203 op_sel_hi:[0,0,0]
	v_mfma_scale_f32_16x16x128_f8f6f4 v[132:135], v[12:19], v[188:195], v[132:135], v202, v203 op_sel_hi:[0,0,0]
	v_mfma_scale_f32_16x16x128_f8f6f4 v[128:131], v[4:11], v[230:237], v[128:131], v202, v203 op_sel_hi:[0,0,0]
	v_mfma_scale_f32_16x16x128_f8f6f4 v[124:127], v[12:19], v[230:237], v[124:127], v202, v203 op_sel_hi:[0,0,0]
	v_mfma_scale_f32_16x16x128_f8f6f4 v[120:123], v[4:11], v[238:245], v[120:123], v202, v203 op_sel_hi:[0,0,0]
	v_mfma_scale_f32_16x16x128_f8f6f4 v[116:119], v[12:19], v[238:245], v[116:119], v202, v203 op_sel_hi:[0,0,0]
	s_barrier
	s_setprio 0
	s_add_i32 s82, s82, 1
	s_lshl_b64 s[2:3], s[82:83], 7
	s_add_u32 s26, s10, s2
	v_mov_b32_e32 v2, v201
	v_readfirstlane_b32 s28, v216
	ds_read_b128 v[180:183], v226 offset:49152
	ds_read_b128 v[184:187], v226 offset:50176
	ds_read_b128 v[188:191], v227 offset:49152
	ds_read_b128 v[192:195], v227 offset:50176
	ds_read_b128 v[230:233], v228 offset:49152
	ds_read_b128 v[234:237], v228 offset:50176
	ds_read_b128 v[238:241], v229 offset:49152
	ds_read_b128 v[242:245], v229 offset:50176
	s_addc_u32 s27, s11, s3
	s_mov_b32 m0, s28
	s_add_u32 s28, s26, 0x10000
	global_load_lds_dwordx4 v2, s[26:27]
	v_mov_b32_e32 v2, v201
	v_readfirstlane_b32 s30, v217
	s_addc_u32 s29, s27, 0
	s_mov_b32 m0, s30
	v_readfirstlane_b32 s30, v220
	global_load_lds_dwordx4 v2, s[28:29]
	s_add_u32 s28, s26, 0x20000
	v_mov_b32_e32 v2, v201
	s_addc_u32 s29, s27, 0
	s_mov_b32 m0, s30
	s_add_u32 s26, s26, 0x30000
	global_load_lds_dwordx4 v2, s[28:29]
	v_mov_b32_e32 v2, v201
	v_readfirstlane_b32 s28, v221
	s_addc_u32 s27, s27, 0
	s_mov_b32 m0, s28
	s_add_u32 s2, s8, s2
	global_load_lds_dwordx4 v2, s[26:27]
	v_mov_b32_e32 v2, v209
	v_readfirstlane_b32 s26, v218
	s_addc_u32 s3, s9, s3
	s_mov_b32 m0, s26
	v_readfirstlane_b32 s26, v219
	global_load_lds_dwordx4 v2, s[2:3]
	v_mov_b32_e32 v2, v210
	s_mov_b32 m0, s26
	s_nop 0
	global_load_lds_dwordx4 v2, s[2:3]
	s_waitcnt vmcnt(8)
	s_waitcnt lgkmcnt(0)
	s_barrier
	s_setprio 1
	v_mfma_scale_f32_16x16x128_f8f6f4 v[112:115], v[20:27], v[180:187], v[112:115], v202, v203 op_sel_hi:[0,0,0]
	v_mfma_scale_f32_16x16x128_f8f6f4 v[108:111], v[28:35], v[180:187], v[108:111], v202, v203 op_sel_hi:[0,0,0]
	v_mfma_scale_f32_16x16x128_f8f6f4 v[104:107], v[20:27], v[188:195], v[104:107], v202, v203 op_sel_hi:[0,0,0]
	v_mfma_scale_f32_16x16x128_f8f6f4 v[100:103], v[28:35], v[188:195], v[100:103], v202, v203 op_sel_hi:[0,0,0]
	v_mfma_scale_f32_16x16x128_f8f6f4 v[96:99], v[20:27], v[230:237], v[96:99], v202, v203 op_sel_hi:[0,0,0]
	v_mfma_scale_f32_16x16x128_f8f6f4 v[92:95], v[28:35], v[230:237], v[92:95], v202, v203 op_sel_hi:[0,0,0]
	v_mfma_scale_f32_16x16x128_f8f6f4 v[88:91], v[20:27], v[238:245], v[88:91], v202, v203 op_sel_hi:[0,0,0]
	v_mfma_scale_f32_16x16x128_f8f6f4 v[84:87], v[28:35], v[238:245], v[84:87], v202, v203 op_sel_hi:[0,0,0]
	v_mfma_scale_f32_16x16x128_f8f6f4 v[80:83], v[4:11], v[180:187], v[80:83], v202, v203 op_sel_hi:[0,0,0]
	v_mfma_scale_f32_16x16x128_f8f6f4 v[76:79], v[12:19], v[180:187], v[76:79], v202, v203 op_sel_hi:[0,0,0]
	v_mfma_scale_f32_16x16x128_f8f6f4 v[72:75], v[4:11], v[188:195], v[72:75], v202, v203 op_sel_hi:[0,0,0]
	v_mfma_scale_f32_16x16x128_f8f6f4 v[68:71], v[12:19], v[188:195], v[68:71], v202, v203 op_sel_hi:[0,0,0]
	v_mfma_scale_f32_16x16x128_f8f6f4 v[64:67], v[4:11], v[230:237], v[64:67], v202, v203 op_sel_hi:[0,0,0]
	v_mfma_scale_f32_16x16x128_f8f6f4 v[60:63], v[12:19], v[230:237], v[60:63], v202, v203 op_sel_hi:[0,0,0]
	v_mfma_scale_f32_16x16x128_f8f6f4 v[56:59], v[4:11], v[238:245], v[56:59], v202, v203 op_sel_hi:[0,0,0]
	v_mfma_scale_f32_16x16x128_f8f6f4 v[52:55], v[12:19], v[238:245], v[52:55], v202, v203 op_sel_hi:[0,0,0]
	s_barrier
	s_setprio 0
	s_add_i32 s25, s25, 2
	s_add_u32 s40, s40, 0x100
	s_addc_u32 s41, s41, 0
	s_cmp_gt_u32 s25, 5
	s_cbranch_scc1 .LBB0_1015

.LBB0_1011:
	ds_read_b128 v[20:23], v222
	ds_read_b128 v[24:27], v222 offset:1024
	ds_read_b128 v[28:31], v222 offset:2048
	ds_read_b128 v[32:35], v222 offset:3072
	ds_read_b128 v[4:7], v223
	ds_read_b128 v[8:11], v223 offset:1024
	ds_read_b128 v[12:15], v223 offset:2048
	ds_read_b128 v[16:19], v223 offset:3072
	v_add_u32_e32 v246, 0xc000, v208
	s_add_u32 s26, s40, 0x80
	v_mov_b32_e32 v2, v211
	v_readfirstlane_b32 s28, v246
	v_add_u32_e32 v246, 0xe000, v208
	ds_read_b128 v[180:183], v226
	ds_read_b128 v[184:187], v226 offset:1024
	ds_read_b128 v[230:233], v227
	ds_read_b128 v[234:237], v227 offset:1024
	ds_read_b128 v[238:241], v228
	ds_read_b128 v[242:245], v228 offset:1024
	ds_read_b128 v[188:191], v229
	ds_read_b128 v[192:195], v229 offset:1024
	s_addc_u32 s27, s41, 0
	s_mov_b32 m0, s28
	v_readfirstlane_b32 s28, v246
	global_load_lds_dwordx4 v2, s[26:27]
	v_mov_b32_e32 v2, v212
	s_mov_b32 m0, s28
	s_nop 0
	global_load_lds_dwordx4 v2, s[26:27]
	s_waitcnt vmcnt(8)
	s_waitcnt lgkmcnt(0)
	s_barrier
	s_setprio 1
	v_mfma_scale_f32_16x16x128_f8f6f4 v[176:179], v[20:27], v[180:187], v[176:179], v202, v203 op_sel_hi:[0,0,0]
	v_mfma_scale_f32_16x16x128_f8f6f4 v[172:175], v[28:35], v[180:187], v[172:175], v202, v203 op_sel_hi:[0,0,0]
	v_mfma_scale_f32_16x16x128_f8f6f4 v[168:171], v[20:27], v[230:237], v[168:171], v202, v203 op_sel_hi:[0,0,0]
	v_mfma_scale_f32_16x16x128_f8f6f4 v[164:167], v[28:35], v[230:237], v[164:167], v202, v203 op_sel_hi:[0,0,0]
	v_mfma_scale_f32_16x16x128_f8f6f4 v[160:163], v[20:27], v[238:245], v[160:163], v202, v203 op_sel_hi:[0,0,0]
	v_mfma_scale_f32_16x16x128_f8f6f4 v[156:159], v[28:35], v[238:245], v[156:159], v202, v203 op_sel_hi:[0,0,0]
	v_mfma_scale_f32_16x16x128_f8f6f4 v[152:155], v[20:27], v[188:195], v[152:155], v202, v203 op_sel_hi:[0,0,0]
	v_mfma_scale_f32_16x16x128_f8f6f4 v[148:151], v[28:35], v[188:195], v[148:151], v202, v203 op_sel_hi:[0,0,0]
	v_mfma_scale_f32_16x16x128_f8f6f4 v[144:147], v[4:11], v[180:187], v[144:147], v202, v203 op_sel_hi:[0,0,0]
	v_mfma_scale_f32_16x16x128_f8f6f4 v[140:143], v[12:19], v[180:187], v[140:143], v202, v203 op_sel_hi:[0,0,0]
	v_mfma_scale_f32_16x16x128_f8f6f4 v[136:139], v[4:11], v[230:237], v[136:139], v202, v203 op_sel_hi:[0,0,0]
	v_mfma_scale_f32_16x16x128_f8f6f4 v[132:135], v[12:19], v[230:237], v[132:135], v202, v203 op_sel_hi:[0,0,0]
	v_mfma_scale_f32_16x16x128_f8f6f4 v[128:131], v[4:11], v[238:245], v[128:131], v202, v203 op_sel_hi:[0,0,0]
	v_mfma_scale_f32_16x16x128_f8f6f4 v[124:127], v[12:19], v[238:245], v[124:127], v202, v203 op_sel_hi:[0,0,0]
	v_mfma_scale_f32_16x16x128_f8f6f4 v[120:123], v[4:11], v[188:195], v[120:123], v202, v203 op_sel_hi:[0,0,0]
	v_mfma_scale_f32_16x16x128_f8f6f4 v[116:119], v[12:19], v[188:195], v[116:119], v202, v203 op_sel_hi:[0,0,0]
	s_barrier
	s_setprio 0
	s_andn2_b64 vcc, exec, s[2:3]
	s_cbranch_vccnz .LBB0_1014
	s_cmpk_gt_u32 s19, 0x1ff
	s_mov_b64 s[20:21], 0
	s_cbranch_scc1 .LBB0_1007
	v_mov_b32_e32 v2, v0
	s_lshr_b32 s3, s19, 3
	v_ashrrev_i32_e32 v181, 31, v2
	v_lshrrev_b32_e32 v181, 26, v181
	v_lshlrev_b32_e32 v180, 4, v2
	v_add_u32_e32 v181, v2, v181
	v_bfe_i32 v2, v2, 27, 1
	v_lshrrev_b32_e32 v2, 22, v2
	v_add_u32_e32 v2, v180, v2
	v_and_b32_e32 v2, 0xfffffc00, v2
	v_sub_u32_e32 v2, v180, v2
	v_lshrrev_b32_e32 v180, 4, v2
	s_add_i32 s6, s18, s19
	s_and_b32 s2, s19, 7
	s_sub_i32 s10, s3, 32
	v_bitop3_b32 v2, v180, v2, 32 bitop3:0x6c
	s_cmpk_lt_u32 s19, 0x100
	v_ashrrev_i32_e32 v182, 31, v2
	s_cselect_b32 s3, s3, s10
	s_lshr_b32 s10, s19, 5
	v_lshrrev_b32_e32 v182, 26, v182
	s_and_b32 s10, s10, 8
	s_and_b32 s11, s3, 7
	v_add_u32_e32 v182, v2, v182
	s_or_b32 s10, s11, s10
	v_lshrrev_b32_e32 v183, 6, v182
	v_and_b32_e32 v182, 0xc0, v182
	s_lshr_b32 s82, s3, 3
	s_lshl_b32 s3, s10, 3
	v_ashrrev_i32_e32 v181, 6, v181
	v_sub_u32_e32 v2, v2, v182
	s_or_b32 s16, s3, s2
	v_lshlrev_b32_e32 v180, 3, v181
	v_lshlrev_b32_e32 v181, 5, v181
	v_ashrrev_i16_sdwa v2, v196, sext(v2) dst_sel:DWORD dst_unused:UNUSED_PAD src0_sel:DWORD src1_sel:BYTE_0
	s_lshl_b64 s[2:3], s[82:83], 18
	v_and_b32_e32 v180, 0x3ffff0, v180
	v_and_b32_e32 v181, 32, v181
	v_bfe_i32 v2, v2, 0, 16
	s_add_u32 s10, s7, s2
	s_addc_u32 s11, s17, s3
	s_lshl_b32 s2, s16, 18
	v_add_lshl_u32 v180, v183, v180, 10
	v_add_lshl_u32 v2, v181, v2, 1
	v_add3_u32 v209, v180, s2, v2
	v_add_u32_e32 v210, 0x10000, v209
	v_add_u32_e32 v211, 0x20000, v209
	v_add_u32_e32 v212, 0x30000, v209
	s_mov_b64 s[20:21], -1
	s_mov_b32 s19, s6
	s_mov_b32 s6, s82
	s_branch .LBB0_1007

.LBB0_1248:
	ds_read_b128 v[20:23], v212
	ds_read_b128 v[24:27], v212 offset:1024
	ds_read_b128 v[28:31], v212 offset:2048
	ds_read_b128 v[32:35], v212 offset:3072
	ds_read_b128 v[4:7], v213
	ds_read_b128 v[8:11], v213 offset:1024
	ds_read_b128 v[12:15], v213 offset:2048
	ds_read_b128 v[16:19], v213 offset:3072
	s_lshl_b32 s2, s30, 7
	s_add_u32 s2, s6, s2
	s_addc_u32 s3, s7, 0
	v_add_u32_e32 v181, 0xc000, v202
	s_add_u32 s2, s2, 0x80
	v_mov_b32_e32 v2, v185
	v_readfirstlane_b32 s31, v181
	v_add_u32_e32 v181, 0xe000, v202
	ds_read_b128 v[220:223], v216
	ds_read_b128 v[224:227], v216 offset:1024
	ds_read_b128 v[228:231], v217
	ds_read_b128 v[232:235], v217 offset:1024
	ds_read_b128 v[236:239], v218
	ds_read_b128 v[240:243], v218 offset:1024
	ds_read_b128 v[244:247], v219
	ds_read_b128 v[248:251], v219 offset:1024
	s_addc_u32 s3, s3, 0
	s_mov_b32 m0, s31
	v_readfirstlane_b32 s31, v181
	global_load_lds_dwordx4 v2, s[2:3]
	v_mov_b32_e32 v2, v186
	s_mov_b32 m0, s31
	s_nop 0
	global_load_lds_dwordx4 v2, s[2:3]
	s_waitcnt vmcnt(8)
	s_waitcnt lgkmcnt(0)
	s_barrier
	s_setprio 1
	v_mfma_scale_f32_16x16x128_f8f6f4 v[176:179], v[20:27], v[220:227], v[176:179], v188, v187 op_sel_hi:[0,0,0]
	v_mfma_scale_f32_16x16x128_f8f6f4 v[168:171], v[28:35], v[220:227], v[168:171], v188, v187 op_sel_hi:[0,0,0]
	v_mfma_scale_f32_16x16x128_f8f6f4 v[160:163], v[20:27], v[228:235], v[160:163], v188, v187 op_sel_hi:[0,0,0]
	v_mfma_scale_f32_16x16x128_f8f6f4 v[152:155], v[28:35], v[228:235], v[152:155], v188, v187 op_sel_hi:[0,0,0]
	v_mfma_scale_f32_16x16x128_f8f6f4 v[144:147], v[20:27], v[236:243], v[144:147], v188, v187 op_sel_hi:[0,0,0]
	v_mfma_scale_f32_16x16x128_f8f6f4 v[136:139], v[28:35], v[236:243], v[136:139], v188, v187 op_sel_hi:[0,0,0]
	v_mfma_scale_f32_16x16x128_f8f6f4 v[128:131], v[20:27], v[244:251], v[128:131], v188, v187 op_sel_hi:[0,0,0]
	v_mfma_scale_f32_16x16x128_f8f6f4 v[120:123], v[28:35], v[244:251], v[120:123], v188, v187 op_sel_hi:[0,0,0]
	s_add_i32 s31, s30, 2
	v_mfma_scale_f32_16x16x128_f8f6f4 v[172:175], v[4:11], v[220:227], v[172:175], v188, v187 op_sel_hi:[0,0,0]
	v_mfma_scale_f32_16x16x128_f8f6f4 v[164:167], v[12:19], v[220:227], v[164:167], v188, v187 op_sel_hi:[0,0,0]
	v_mfma_scale_f32_16x16x128_f8f6f4 v[156:159], v[4:11], v[228:235], v[156:159], v188, v187 op_sel_hi:[0,0,0]
	v_mfma_scale_f32_16x16x128_f8f6f4 v[148:151], v[12:19], v[228:235], v[148:151], v188, v187 op_sel_hi:[0,0,0]
	v_mfma_scale_f32_16x16x128_f8f6f4 v[140:143], v[4:11], v[236:243], v[140:143], v188, v187 op_sel_hi:[0,0,0]
	v_mfma_scale_f32_16x16x128_f8f6f4 v[132:135], v[12:19], v[236:243], v[132:135], v188, v187 op_sel_hi:[0,0,0]
	v_mfma_scale_f32_16x16x128_f8f6f4 v[124:127], v[4:11], v[244:251], v[124:127], v188, v187 op_sel_hi:[0,0,0]
	v_mfma_scale_f32_16x16x128_f8f6f4 v[116:119], v[12:19], v[244:251], v[116:119], v188, v187 op_sel_hi:[0,0,0]
	s_cmp_lg_u32 s30, 6
	s_barrier
	s_setprio 0
	s_cbranch_scc1 .LBB0_1253
	s_mov_b64 s[2:3], -1
	s_cmp_ge_u32 s18, s16
	s_mov_b64 s[12:13], -1
	s_cbranch_scc1 .LBB0_1251

.LBB0_1259:
	s_lshl_b64 s[2:3], s[82:83], 7
	s_add_u32 s34, s4, s2
	v_mov_b32_e32 v2, v184
	v_readfirstlane_b32 s33, v189
	ds_read_b128 v[220:223], v216 offset:16384
	ds_read_b128 v[224:227], v216 offset:17408
	ds_read_b128 v[228:231], v217 offset:16384
	ds_read_b128 v[232:235], v217 offset:17408
	ds_read_b128 v[236:239], v218 offset:16384
	ds_read_b128 v[240:243], v218 offset:17408
	ds_read_b128 v[244:247], v219 offset:16384
	ds_read_b128 v[248:251], v219 offset:17408
	s_addc_u32 s35, s5, s3
	s_mov_b32 m0, s33
	s_add_u32 s40, s34, 0x10000
	global_load_lds_dwordx4 v2, s[34:35]
	v_mov_b32_e32 v2, v184
	v_readfirstlane_b32 s33, v190
	s_addc_u32 s41, s35, 0
	s_mov_b32 m0, s33
	v_readfirstlane_b32 s33, v191
	global_load_lds_dwordx4 v2, s[40:41]
	s_add_u32 s40, s34, 0x20000
	v_mov_b32_e32 v2, v184
	s_addc_u32 s41, s35, 0
	s_mov_b32 m0, s33
	s_add_u32 s34, s34, 0x30000
	global_load_lds_dwordx4 v2, s[40:41]
	v_mov_b32_e32 v2, v184
	v_readfirstlane_b32 s33, v201
	s_addc_u32 s35, s35, 0
	s_mov_b32 m0, s33
	s_add_u32 s2, s6, s2
	global_load_lds_dwordx4 v2, s[34:35]
	v_mov_b32_e32 v2, v182
	v_readfirstlane_b32 s33, v202
	s_addc_u32 s3, s7, s3
	s_mov_b32 m0, s33
	v_readfirstlane_b32 s33, v203
	global_load_lds_dwordx4 v2, s[2:3]
	v_mov_b32_e32 v2, v183
	s_mov_b32 m0, s33
	s_nop 0
	global_load_lds_dwordx4 v2, s[2:3]
	s_waitcnt vmcnt(8)
	s_waitcnt lgkmcnt(0)
	s_barrier
	s_setprio 1
	v_mfma_scale_f32_16x16x128_f8f6f4 v[112:115], v[20:27], v[220:227], v[112:115], v188, v187 op_sel_hi:[0,0,0]
	v_mfma_scale_f32_16x16x128_f8f6f4 v[104:107], v[28:35], v[220:227], v[104:107], v188, v187 op_sel_hi:[0,0,0]
	v_mfma_scale_f32_16x16x128_f8f6f4 v[96:99], v[20:27], v[228:235], v[96:99], v188, v187 op_sel_hi:[0,0,0]
	v_mfma_scale_f32_16x16x128_f8f6f4 v[88:91], v[28:35], v[228:235], v[88:91], v188, v187 op_sel_hi:[0,0,0]
	v_mfma_scale_f32_16x16x128_f8f6f4 v[80:83], v[20:27], v[236:243], v[80:83], v188, v187 op_sel_hi:[0,0,0]
	v_mfma_scale_f32_16x16x128_f8f6f4 v[72:75], v[28:35], v[236:243], v[72:75], v188, v187 op_sel_hi:[0,0,0]
	v_mfma_scale_f32_16x16x128_f8f6f4 v[64:67], v[20:27], v[244:251], v[64:67], v188, v187 op_sel_hi:[0,0,0]
	v_mfma_scale_f32_16x16x128_f8f6f4 v[56:59], v[28:35], v[244:251], v[56:59], v188, v187 op_sel_hi:[0,0,0]
	v_mfma_scale_f32_16x16x128_f8f6f4 v[108:111], v[4:11], v[220:227], v[108:111], v188, v187 op_sel_hi:[0,0,0]
	v_mfma_scale_f32_16x16x128_f8f6f4 v[100:103], v[12:19], v[220:227], v[100:103], v188, v187 op_sel_hi:[0,0,0]
	v_mfma_scale_f32_16x16x128_f8f6f4 v[92:95], v[4:11], v[228:235], v[92:95], v188, v187 op_sel_hi:[0,0,0]
	v_mfma_scale_f32_16x16x128_f8f6f4 v[84:87], v[12:19], v[228:235], v[84:87], v188, v187 op_sel_hi:[0,0,0]
	v_mfma_scale_f32_16x16x128_f8f6f4 v[76:79], v[4:11], v[236:243], v[76:79], v188, v187 op_sel_hi:[0,0,0]
	v_mfma_scale_f32_16x16x128_f8f6f4 v[68:71], v[12:19], v[236:243], v[68:71], v188, v187 op_sel_hi:[0,0,0]
	v_mfma_scale_f32_16x16x128_f8f6f4 v[60:63], v[4:11], v[244:251], v[60:63], v188, v187 op_sel_hi:[0,0,0]
	v_mfma_scale_f32_16x16x128_f8f6f4 v[52:55], v[12:19], v[244:251], v[52:55], v188, v187 op_sel_hi:[0,0,0]
	s_barrier
	s_setprio 0
	ds_read_b128 v[20:23], v214
	ds_read_b128 v[24:27], v214 offset:1024
	ds_read_b128 v[28:31], v214 offset:2048
	ds_read_b128 v[32:35], v214 offset:3072
	ds_read_b128 v[4:7], v215
	ds_read_b128 v[8:11], v215 offset:1024
	ds_read_b128 v[12:15], v215 offset:2048
	ds_read_b128 v[16:19], v215 offset:3072
	v_mov_b32_e32 v2, v185
	v_readfirstlane_b32 s33, v204
	ds_read_b128 v[220:223], v216 offset:32768
	ds_read_b128 v[224:227], v216 offset:33792
	ds_read_b128 v[228:231], v217 offset:32768
	ds_read_b128 v[232:235], v217 offset:33792
	ds_read_b128 v[236:239], v218 offset:32768
	ds_read_b128 v[240:243], v218 offset:33792
	ds_read_b128 v[244:247], v219 offset:32768
	ds_read_b128 v[248:251], v219 offset:33792
	s_mov_b32 m0, s33
	v_readfirstlane_b32 s33, v205
	global_load_lds_dwordx4 v2, s[2:3]
	v_mov_b32_e32 v2, v186
	s_mov_b32 m0, s33
	s_nop 0
	global_load_lds_dwordx4 v2, s[2:3]
	s_waitcnt vmcnt(8)
	s_waitcnt lgkmcnt(0)
	s_barrier
	s_setprio 1
	v_mfma_scale_f32_16x16x128_f8f6f4 v[176:179], v[20:27], v[220:227], v[176:179], v188, v187 op_sel_hi:[0,0,0]
	v_mfma_scale_f32_16x16x128_f8f6f4 v[168:171], v[28:35], v[220:227], v[168:171], v188, v187 op_sel_hi:[0,0,0]
	v_mfma_scale_f32_16x16x128_f8f6f4 v[160:163], v[20:27], v[228:235], v[160:163], v188, v187 op_sel_hi:[0,0,0]
	v_mfma_scale_f32_16x16x128_f8f6f4 v[152:155], v[28:35], v[228:235], v[152:155], v188, v187 op_sel_hi:[0,0,0]
	v_mfma_scale_f32_16x16x128_f8f6f4 v[144:147], v[20:27], v[236:243], v[144:147], v188, v187 op_sel_hi:[0,0,0]
	v_mfma_scale_f32_16x16x128_f8f6f4 v[136:139], v[28:35], v[236:243], v[136:139], v188, v187 op_sel_hi:[0,0,0]
	v_mfma_scale_f32_16x16x128_f8f6f4 v[128:131], v[20:27], v[244:251], v[128:131], v188, v187 op_sel_hi:[0,0,0]
	v_mfma_scale_f32_16x16x128_f8f6f4 v[120:123], v[28:35], v[244:251], v[120:123], v188, v187 op_sel_hi:[0,0,0]
	v_mfma_scale_f32_16x16x128_f8f6f4 v[172:175], v[4:11], v[220:227], v[172:175], v188, v187 op_sel_hi:[0,0,0]
	v_mfma_scale_f32_16x16x128_f8f6f4 v[164:167], v[12:19], v[220:227], v[164:167], v188, v187 op_sel_hi:[0,0,0]
	v_mfma_scale_f32_16x16x128_f8f6f4 v[156:159], v[4:11], v[228:235], v[156:159], v188, v187 op_sel_hi:[0,0,0]
	v_mfma_scale_f32_16x16x128_f8f6f4 v[148:151], v[12:19], v[228:235], v[148:151], v188, v187 op_sel_hi:[0,0,0]
	v_mfma_scale_f32_16x16x128_f8f6f4 v[140:143], v[4:11], v[236:243], v[140:143], v188, v187 op_sel_hi:[0,0,0]
	v_mfma_scale_f32_16x16x128_f8f6f4 v[132:135], v[12:19], v[236:243], v[132:135], v188, v187 op_sel_hi:[0,0,0]
	v_mfma_scale_f32_16x16x128_f8f6f4 v[124:127], v[4:11], v[244:251], v[124:127], v188, v187 op_sel_hi:[0,0,0]
	v_mfma_scale_f32_16x16x128_f8f6f4 v[116:119], v[12:19], v[244:251], v[116:119], v188, v187 op_sel_hi:[0,0,0]
	s_barrier
	s_setprio 0
	s_add_i32 s82, s82, 1
	s_lshl_b64 s[2:3], s[82:83], 7
	s_add_u32 s34, s4, s2
	v_mov_b32_e32 v2, v184
	v_readfirstlane_b32 s33, v206
	ds_read_b128 v[220:223], v216 offset:49152
	ds_read_b128 v[224:227], v216 offset:50176
	ds_read_b128 v[228:231], v217 offset:49152
	ds_read_b128 v[232:235], v217 offset:50176
	ds_read_b128 v[236:239], v218 offset:49152
	ds_read_b128 v[240:243], v218 offset:50176
	ds_read_b128 v[244:247], v219 offset:49152
	ds_read_b128 v[248:251], v219 offset:50176
	s_addc_u32 s35, s5, s3
	s_mov_b32 m0, s33
	s_add_u32 s40, s34, 0x10000
	global_load_lds_dwordx4 v2, s[34:35]
	v_mov_b32_e32 v2, v184
	v_readfirstlane_b32 s33, v207
	s_addc_u32 s41, s35, 0
	s_mov_b32 m0, s33
	v_readfirstlane_b32 s33, v210
	global_load_lds_dwordx4 v2, s[40:41]
	s_add_u32 s40, s34, 0x20000
	v_mov_b32_e32 v2, v184
	s_addc_u32 s41, s35, 0
	s_mov_b32 m0, s33
	s_add_u32 s34, s34, 0x30000
	global_load_lds_dwordx4 v2, s[40:41]
	v_mov_b32_e32 v2, v184
	v_readfirstlane_b32 s33, v211
	s_addc_u32 s35, s35, 0
	s_mov_b32 m0, s33
	s_add_u32 s2, s6, s2
	global_load_lds_dwordx4 v2, s[34:35]
	v_mov_b32_e32 v2, v182
	v_readfirstlane_b32 s33, v208
	s_addc_u32 s3, s7, s3
	s_mov_b32 m0, s33
	v_readfirstlane_b32 s33, v209
	global_load_lds_dwordx4 v2, s[2:3]
	v_mov_b32_e32 v2, v183
	s_mov_b32 m0, s33
	s_nop 0
	global_load_lds_dwordx4 v2, s[2:3]
	s_waitcnt vmcnt(8)
	s_waitcnt lgkmcnt(0)
	s_barrier
	s_setprio 1
	v_mfma_scale_f32_16x16x128_f8f6f4 v[112:115], v[20:27], v[220:227], v[112:115], v188, v187 op_sel_hi:[0,0,0]
	v_mfma_scale_f32_16x16x128_f8f6f4 v[104:107], v[28:35], v[220:227], v[104:107], v188, v187 op_sel_hi:[0,0,0]
	v_mfma_scale_f32_16x16x128_f8f6f4 v[96:99], v[20:27], v[228:235], v[96:99], v188, v187 op_sel_hi:[0,0,0]
	v_mfma_scale_f32_16x16x128_f8f6f4 v[88:91], v[28:35], v[228:235], v[88:91], v188, v187 op_sel_hi:[0,0,0]
	v_mfma_scale_f32_16x16x128_f8f6f4 v[80:83], v[20:27], v[236:243], v[80:83], v188, v187 op_sel_hi:[0,0,0]
	v_mfma_scale_f32_16x16x128_f8f6f4 v[72:75], v[28:35], v[236:243], v[72:75], v188, v187 op_sel_hi:[0,0,0]
	v_mfma_scale_f32_16x16x128_f8f6f4 v[64:67], v[20:27], v[244:251], v[64:67], v188, v187 op_sel_hi:[0,0,0]
	v_mfma_scale_f32_16x16x128_f8f6f4 v[56:59], v[28:35], v[244:251], v[56:59], v188, v187 op_sel_hi:[0,0,0]
	v_mfma_scale_f32_16x16x128_f8f6f4 v[108:111], v[4:11], v[220:227], v[108:111], v188, v187 op_sel_hi:[0,0,0]
	v_mfma_scale_f32_16x16x128_f8f6f4 v[100:103], v[12:19], v[220:227], v[100:103], v188, v187 op_sel_hi:[0,0,0]
	v_mfma_scale_f32_16x16x128_f8f6f4 v[92:95], v[4:11], v[228:235], v[92:95], v188, v187 op_sel_hi:[0,0,0]
	v_mfma_scale_f32_16x16x128_f8f6f4 v[84:87], v[12:19], v[228:235], v[84:87], v188, v187 op_sel_hi:[0,0,0]
	v_mfma_scale_f32_16x16x128_f8f6f4 v[76:79], v[4:11], v[236:243], v[76:79], v188, v187 op_sel_hi:[0,0,0]
	v_mfma_scale_f32_16x16x128_f8f6f4 v[68:71], v[12:19], v[236:243], v[68:71], v188, v187 op_sel_hi:[0,0,0]
	v_mfma_scale_f32_16x16x128_f8f6f4 v[60:63], v[4:11], v[244:251], v[60:63], v188, v187 op_sel_hi:[0,0,0]
	v_mfma_scale_f32_16x16x128_f8f6f4 v[52:55], v[12:19], v[244:251], v[52:55], v188, v187 op_sel_hi:[0,0,0]
	s_barrier
	s_setprio 0
	s_cmp_gt_u32 s30, 5
	s_cbranch_scc1 .LBB0_1261
	s_mov_b32 s30, s31
	s_branch .LBB0_1248

.LBB0_1387:
	ds_read_b128 v[20:23], v212
	ds_read_b128 v[24:27], v212 offset:1024
	ds_read_b128 v[28:31], v212 offset:2048
	ds_read_b128 v[32:35], v212 offset:3072
	ds_read_b128 v[4:7], v213
	ds_read_b128 v[8:11], v213 offset:1024
	ds_read_b128 v[12:15], v213 offset:2048
	ds_read_b128 v[16:19], v213 offset:3072
	s_lshl_b32 s2, s23, 7
	s_add_u32 s2, s4, s2
	s_addc_u32 s3, s5, 0
	v_add_u32_e32 v181, 0xc000, v202
	s_add_u32 s2, s2, 0x80
	v_mov_b32_e32 v2, v184
	v_readfirstlane_b32 s24, v181
	v_add_u32_e32 v181, 0xe000, v202
	ds_read_b128 v[222:225], v216
	ds_read_b128 v[226:229], v216 offset:1024
	ds_read_b128 v[230:233], v217
	ds_read_b128 v[234:237], v217 offset:1024
	ds_read_b128 v[238:241], v218
	ds_read_b128 v[242:245], v218 offset:1024
	ds_read_b128 v[36:39], v219
	ds_read_b128 v[40:43], v219 offset:1024
	s_addc_u32 s3, s3, 0
	s_mov_b32 m0, s24
	v_readfirstlane_b32 s24, v181
	global_load_lds_dwordx4 v2, s[2:3]
	v_mov_b32_e32 v2, v185
	s_mov_b32 m0, s24
	s_nop 0
	global_load_lds_dwordx4 v2, s[2:3]
	s_waitcnt vmcnt(8)
	s_waitcnt lgkmcnt(0)
	s_barrier
	s_setprio 1
	v_mfma_scale_f32_16x16x128_f8f6f4 v[176:179], v[20:27], v[222:229], v[176:179], v188, v187 op_sel_hi:[0,0,0]
	v_mfma_scale_f32_16x16x128_f8f6f4 v[172:175], v[28:35], v[222:229], v[172:175], v188, v187 op_sel_hi:[0,0,0]
	v_mfma_scale_f32_16x16x128_f8f6f4 v[168:171], v[20:27], v[230:237], v[168:171], v188, v187 op_sel_hi:[0,0,0]
	v_mfma_scale_f32_16x16x128_f8f6f4 v[164:167], v[28:35], v[230:237], v[164:167], v188, v187 op_sel_hi:[0,0,0]
	v_mfma_scale_f32_16x16x128_f8f6f4 v[160:163], v[20:27], v[238:245], v[160:163], v188, v187 op_sel_hi:[0,0,0]
	v_mfma_scale_f32_16x16x128_f8f6f4 v[156:159], v[28:35], v[238:245], v[156:159], v188, v187 op_sel_hi:[0,0,0]
	v_mfma_scale_f32_16x16x128_f8f6f4 v[152:155], v[20:27], v[36:43], v[152:155], v188, v187 op_sel_hi:[0,0,0]
	v_mfma_scale_f32_16x16x128_f8f6f4 v[148:151], v[28:35], v[36:43], v[148:151], v188, v187 op_sel_hi:[0,0,0]
	s_add_i32 s24, s23, 2
	v_mfma_scale_f32_16x16x128_f8f6f4 v[120:123], v[4:11], v[222:229], v[120:123], v188, v187 op_sel_hi:[0,0,0]
	v_mfma_scale_f32_16x16x128_f8f6f4 v[116:119], v[12:19], v[222:229], v[116:119], v188, v187 op_sel_hi:[0,0,0]
	v_mfma_scale_f32_16x16x128_f8f6f4 v[112:115], v[4:11], v[230:237], v[112:115], v188, v187 op_sel_hi:[0,0,0]
	v_mfma_scale_f32_16x16x128_f8f6f4 v[108:111], v[12:19], v[230:237], v[108:111], v188, v187 op_sel_hi:[0,0,0]
	v_mfma_scale_f32_16x16x128_f8f6f4 v[96:99], v[4:11], v[238:245], v[96:99], v188, v187 op_sel_hi:[0,0,0]
	v_mfma_scale_f32_16x16x128_f8f6f4 v[92:95], v[12:19], v[238:245], v[92:95], v188, v187 op_sel_hi:[0,0,0]
	v_mfma_scale_f32_16x16x128_f8f6f4 v[88:91], v[4:11], v[36:43], v[88:91], v188, v187 op_sel_hi:[0,0,0]
	v_mfma_scale_f32_16x16x128_f8f6f4 v[84:87], v[12:19], v[36:43], v[84:87], v188, v187 op_sel_hi:[0,0,0]
	s_cmp_lg_u32 s23, 6
	s_barrier
	s_setprio 0
	s_cbranch_scc1 .LBB0_1392
	s_mov_b64 s[2:3], -1
	s_cmp_ge_u32 s14, s13
	s_mov_b64 s[10:11], -1
	s_cbranch_scc1 .LBB0_1390

.LBB0_1398:
	s_lshl_b64 s[2:3], s[82:83], 7
	s_add_u32 s26, s6, s2
	v_mov_b32_e32 v2, v186
	v_readfirstlane_b32 s25, v189
	ds_read_b128 v[36:39], v216 offset:16384
	ds_read_b128 v[40:43], v216 offset:17408
	ds_read_b128 v[222:225], v217 offset:16384
	ds_read_b128 v[226:229], v217 offset:17408
	ds_read_b128 v[230:233], v218 offset:16384
	ds_read_b128 v[234:237], v218 offset:17408
	ds_read_b128 v[238:241], v219 offset:16384
	ds_read_b128 v[242:245], v219 offset:17408
	s_addc_u32 s27, s7, s3
	s_mov_b32 m0, s25
	s_add_u32 s28, s26, 0x10000
	global_load_lds_dwordx4 v2, s[26:27]
	v_mov_b32_e32 v2, v186
	v_readfirstlane_b32 s25, v190
	s_addc_u32 s29, s27, 0
	s_mov_b32 m0, s25
	v_readfirstlane_b32 s25, v191
	global_load_lds_dwordx4 v2, s[28:29]
	s_add_u32 s28, s26, 0x20000
	v_mov_b32_e32 v2, v186
	s_addc_u32 s29, s27, 0
	s_mov_b32 m0, s25
	s_add_u32 s26, s26, 0x30000
	global_load_lds_dwordx4 v2, s[28:29]
	v_mov_b32_e32 v2, v186
	v_readfirstlane_b32 s25, v201
	s_addc_u32 s27, s27, 0
	s_mov_b32 m0, s25
	s_add_u32 s2, s4, s2
	global_load_lds_dwordx4 v2, s[26:27]
	v_mov_b32_e32 v2, v182
	v_readfirstlane_b32 s25, v202
	s_addc_u32 s3, s5, s3
	s_mov_b32 m0, s25
	v_readfirstlane_b32 s25, v203
	global_load_lds_dwordx4 v2, s[2:3]
	v_mov_b32_e32 v2, v183
	s_mov_b32 m0, s25
	s_nop 0
	global_load_lds_dwordx4 v2, s[2:3]
	s_waitcnt vmcnt(8)
	s_waitcnt lgkmcnt(0)
	s_barrier
	s_setprio 1
	v_mfma_scale_f32_16x16x128_f8f6f4 v[144:147], v[20:27], v[36:43], v[144:147], v188, v187 op_sel_hi:[0,0,0]
	v_mfma_scale_f32_16x16x128_f8f6f4 v[140:143], v[28:35], v[36:43], v[140:143], v188, v187 op_sel_hi:[0,0,0]
	v_mfma_scale_f32_16x16x128_f8f6f4 v[136:139], v[20:27], v[222:229], v[136:139], v188, v187 op_sel_hi:[0,0,0]
	v_mfma_scale_f32_16x16x128_f8f6f4 v[132:135], v[28:35], v[222:229], v[132:135], v188, v187 op_sel_hi:[0,0,0]
	v_mfma_scale_f32_16x16x128_f8f6f4 v[128:131], v[20:27], v[230:237], v[128:131], v188, v187 op_sel_hi:[0,0,0]
	v_mfma_scale_f32_16x16x128_f8f6f4 v[124:127], v[28:35], v[230:237], v[124:127], v188, v187 op_sel_hi:[0,0,0]
	v_mfma_scale_f32_16x16x128_f8f6f4 v[100:103], v[20:27], v[238:245], v[100:103], v188, v187 op_sel_hi:[0,0,0]
	v_mfma_scale_f32_16x16x128_f8f6f4 v[104:107], v[28:35], v[238:245], v[104:107], v188, v187 op_sel_hi:[0,0,0]
	v_mfma_scale_f32_16x16x128_f8f6f4 v[80:83], v[4:11], v[36:43], v[80:83], v188, v187 op_sel_hi:[0,0,0]
	v_mfma_scale_f32_16x16x128_f8f6f4 v[76:79], v[12:19], v[36:43], v[76:79], v188, v187 op_sel_hi:[0,0,0]
	v_mfma_scale_f32_16x16x128_f8f6f4 v[72:75], v[4:11], v[222:229], v[72:75], v188, v187 op_sel_hi:[0,0,0]
	v_mfma_scale_f32_16x16x128_f8f6f4 v[68:71], v[12:19], v[222:229], v[68:71], v188, v187 op_sel_hi:[0,0,0]
	v_mfma_scale_f32_16x16x128_f8f6f4 v[64:67], v[4:11], v[230:237], v[64:67], v188, v187 op_sel_hi:[0,0,0]
	v_mfma_scale_f32_16x16x128_f8f6f4 v[60:63], v[12:19], v[230:237], v[60:63], v188, v187 op_sel_hi:[0,0,0]
	v_mfma_scale_f32_16x16x128_f8f6f4 v[52:55], v[4:11], v[238:245], v[52:55], v188, v187 op_sel_hi:[0,0,0]
	v_mfma_scale_f32_16x16x128_f8f6f4 v[56:59], v[12:19], v[238:245], v[56:59], v188, v187 op_sel_hi:[0,0,0]
	s_barrier
	s_setprio 0
	ds_read_b128 v[20:23], v214
	ds_read_b128 v[24:27], v214 offset:1024
	ds_read_b128 v[28:31], v214 offset:2048
	ds_read_b128 v[32:35], v214 offset:3072
	ds_read_b128 v[4:7], v215
	ds_read_b128 v[8:11], v215 offset:1024
	ds_read_b128 v[12:15], v215 offset:2048
	ds_read_b128 v[16:19], v215 offset:3072
	v_mov_b32_e32 v2, v184
	v_readfirstlane_b32 s25, v204
	ds_read_b128 v[36:39], v216 offset:32768
	ds_read_b128 v[40:43], v216 offset:33792
	ds_read_b128 v[222:225], v217 offset:32768
	ds_read_b128 v[226:229], v217 offset:33792
	ds_read_b128 v[230:233], v218 offset:32768
	ds_read_b128 v[234:237], v218 offset:33792
	ds_read_b128 v[238:241], v219 offset:32768
	ds_read_b128 v[242:245], v219 offset:33792
	s_mov_b32 m0, s25
	v_readfirstlane_b32 s25, v205
	global_load_lds_dwordx4 v2, s[2:3]
	v_mov_b32_e32 v2, v185
	s_mov_b32 m0, s25
	s_nop 0
	global_load_lds_dwordx4 v2, s[2:3]
	s_waitcnt vmcnt(8)
	s_waitcnt lgkmcnt(0)
	s_barrier
	s_setprio 1
	v_mfma_scale_f32_16x16x128_f8f6f4 v[176:179], v[20:27], v[36:43], v[176:179], v188, v187 op_sel_hi:[0,0,0]
	v_mfma_scale_f32_16x16x128_f8f6f4 v[172:175], v[28:35], v[36:43], v[172:175], v188, v187 op_sel_hi:[0,0,0]
	v_mfma_scale_f32_16x16x128_f8f6f4 v[168:171], v[20:27], v[222:229], v[168:171], v188, v187 op_sel_hi:[0,0,0]
	v_mfma_scale_f32_16x16x128_f8f6f4 v[164:167], v[28:35], v[222:229], v[164:167], v188, v187 op_sel_hi:[0,0,0]
	v_mfma_scale_f32_16x16x128_f8f6f4 v[160:163], v[20:27], v[230:237], v[160:163], v188, v187 op_sel_hi:[0,0,0]
	v_mfma_scale_f32_16x16x128_f8f6f4 v[156:159], v[28:35], v[230:237], v[156:159], v188, v187 op_sel_hi:[0,0,0]
	v_mfma_scale_f32_16x16x128_f8f6f4 v[152:155], v[20:27], v[238:245], v[152:155], v188, v187 op_sel_hi:[0,0,0]
	v_mfma_scale_f32_16x16x128_f8f6f4 v[148:151], v[28:35], v[238:245], v[148:151], v188, v187 op_sel_hi:[0,0,0]
	v_mfma_scale_f32_16x16x128_f8f6f4 v[120:123], v[4:11], v[36:43], v[120:123], v188, v187 op_sel_hi:[0,0,0]
	v_mfma_scale_f32_16x16x128_f8f6f4 v[116:119], v[12:19], v[36:43], v[116:119], v188, v187 op_sel_hi:[0,0,0]
	v_mfma_scale_f32_16x16x128_f8f6f4 v[112:115], v[4:11], v[222:229], v[112:115], v188, v187 op_sel_hi:[0,0,0]
	v_mfma_scale_f32_16x16x128_f8f6f4 v[108:111], v[12:19], v[222:229], v[108:111], v188, v187 op_sel_hi:[0,0,0]
	v_mfma_scale_f32_16x16x128_f8f6f4 v[96:99], v[4:11], v[230:237], v[96:99], v188, v187 op_sel_hi:[0,0,0]
	v_mfma_scale_f32_16x16x128_f8f6f4 v[92:95], v[12:19], v[230:237], v[92:95], v188, v187 op_sel_hi:[0,0,0]
	v_mfma_scale_f32_16x16x128_f8f6f4 v[88:91], v[4:11], v[238:245], v[88:91], v188, v187 op_sel_hi:[0,0,0]
	v_mfma_scale_f32_16x16x128_f8f6f4 v[84:87], v[12:19], v[238:245], v[84:87], v188, v187 op_sel_hi:[0,0,0]
	s_barrier
	s_setprio 0
	s_add_i32 s82, s82, 1
	s_lshl_b64 s[2:3], s[82:83], 7
	s_add_u32 s26, s6, s2
	v_mov_b32_e32 v2, v186
	v_readfirstlane_b32 s25, v206
	ds_read_b128 v[36:39], v216 offset:49152
	ds_read_b128 v[40:43], v216 offset:50176
	ds_read_b128 v[222:225], v217 offset:49152
	ds_read_b128 v[226:229], v217 offset:50176
	ds_read_b128 v[230:233], v218 offset:49152
	ds_read_b128 v[234:237], v218 offset:50176
	ds_read_b128 v[238:241], v219 offset:49152
	ds_read_b128 v[242:245], v219 offset:50176
	s_addc_u32 s27, s7, s3
	s_mov_b32 m0, s25
	s_add_u32 s28, s26, 0x10000
	global_load_lds_dwordx4 v2, s[26:27]
	v_mov_b32_e32 v2, v186
	v_readfirstlane_b32 s25, v207
	s_addc_u32 s29, s27, 0
	s_mov_b32 m0, s25
	v_readfirstlane_b32 s25, v210
	global_load_lds_dwordx4 v2, s[28:29]
	s_add_u32 s28, s26, 0x20000
	v_mov_b32_e32 v2, v186
	s_addc_u32 s29, s27, 0
	s_mov_b32 m0, s25
	s_add_u32 s26, s26, 0x30000
	global_load_lds_dwordx4 v2, s[28:29]
	v_mov_b32_e32 v2, v186
	v_readfirstlane_b32 s25, v211
	s_addc_u32 s27, s27, 0
	s_mov_b32 m0, s25
	s_add_u32 s2, s4, s2
	global_load_lds_dwordx4 v2, s[26:27]
	v_mov_b32_e32 v2, v182
	v_readfirstlane_b32 s25, v208
	s_addc_u32 s3, s5, s3
	s_mov_b32 m0, s25
	v_readfirstlane_b32 s25, v209
	global_load_lds_dwordx4 v2, s[2:3]
	v_mov_b32_e32 v2, v183
	s_mov_b32 m0, s25
	s_nop 0
	global_load_lds_dwordx4 v2, s[2:3]
	s_waitcnt vmcnt(8)
	s_waitcnt lgkmcnt(0)
	s_barrier
	s_setprio 1
	v_mfma_scale_f32_16x16x128_f8f6f4 v[144:147], v[20:27], v[36:43], v[144:147], v188, v187 op_sel_hi:[0,0,0]
	v_mfma_scale_f32_16x16x128_f8f6f4 v[140:143], v[28:35], v[36:43], v[140:143], v188, v187 op_sel_hi:[0,0,0]
	v_mfma_scale_f32_16x16x128_f8f6f4 v[136:139], v[20:27], v[222:229], v[136:139], v188, v187 op_sel_hi:[0,0,0]
	v_mfma_scale_f32_16x16x128_f8f6f4 v[132:135], v[28:35], v[222:229], v[132:135], v188, v187 op_sel_hi:[0,0,0]
	v_mfma_scale_f32_16x16x128_f8f6f4 v[128:131], v[20:27], v[230:237], v[128:131], v188, v187 op_sel_hi:[0,0,0]
	v_mfma_scale_f32_16x16x128_f8f6f4 v[124:127], v[28:35], v[230:237], v[124:127], v188, v187 op_sel_hi:[0,0,0]
	v_mfma_scale_f32_16x16x128_f8f6f4 v[100:103], v[20:27], v[238:245], v[100:103], v188, v187 op_sel_hi:[0,0,0]
	v_mfma_scale_f32_16x16x128_f8f6f4 v[104:107], v[28:35], v[238:245], v[104:107], v188, v187 op_sel_hi:[0,0,0]
	v_mfma_scale_f32_16x16x128_f8f6f4 v[80:83], v[4:11], v[36:43], v[80:83], v188, v187 op_sel_hi:[0,0,0]
	v_mfma_scale_f32_16x16x128_f8f6f4 v[76:79], v[12:19], v[36:43], v[76:79], v188, v187 op_sel_hi:[0,0,0]
	v_mfma_scale_f32_16x16x128_f8f6f4 v[72:75], v[4:11], v[222:229], v[72:75], v188, v187 op_sel_hi:[0,0,0]
	v_mfma_scale_f32_16x16x128_f8f6f4 v[68:71], v[12:19], v[222:229], v[68:71], v188, v187 op_sel_hi:[0,0,0]
	v_mfma_scale_f32_16x16x128_f8f6f4 v[64:67], v[4:11], v[230:237], v[64:67], v188, v187 op_sel_hi:[0,0,0]
	v_mfma_scale_f32_16x16x128_f8f6f4 v[60:63], v[12:19], v[230:237], v[60:63], v188, v187 op_sel_hi:[0,0,0]
	v_mfma_scale_f32_16x16x128_f8f6f4 v[52:55], v[4:11], v[238:245], v[52:55], v188, v187 op_sel_hi:[0,0,0]
	v_mfma_scale_f32_16x16x128_f8f6f4 v[56:59], v[12:19], v[238:245], v[56:59], v188, v187 op_sel_hi:[0,0,0]
	s_barrier
	s_setprio 0
	s_cmp_gt_u32 s23, 5
	s_cbranch_scc1 .LBB0_1400
	s_mov_b32 s23, s24
	s_branch .LBB0_1387
